# v85 with the P11 sort stages' spare register moved off v254 (v254 holds lane-parked scalars read by the grid-barrier init path): same instruction streams otherwise
# speedup vs baseline: 1.0176x; 1.0098x over previous
; __device__ __forceinline__ void p11_route(Frame& F) {
;     ...
;     for (int item = F.gw; item < (S_ / 16) * PH; item += F.NGW) {
;         const int tile = item >> 3, h = item & 7, t0 = tile * 16;
; #pragma unroll
;         for (int c = 0; c < 2; ++c) {
;             f32x4 acc[8];
; #pragma unroll
;             for (int nt = 0; nt < 8; ++nt) acc[nt] = (f32x4){0.f, 0.f, 0.f, 0.f};
; #pragma unroll
;             for (int ks = 0; ks < 4; ++ks) { const gbf16x8 a = *(const gbf16x8*)(QRY + (size_t)(t0 + l15) * 2048 + h * 256 + c * 128 + 32 * ks + 8 * g);
; #pragma unroll
;                 for (int nt = 0; nt < 8; ++nt) acc[nt] = __builtin_amdgcn_mfma_f32_16x16x32_bf16(a, *(const gbf16x8*)(SK + ((size_t)(h * 2 + c) * PNK + 16 * nt + l15) * 128 + 32 * ks + 8 * g), acc[nt], 0, 0, 0); }
; #pragma unroll
;             for (int nt = 0; nt < 8; ++nt)
; #pragma unroll
;                 for (int r = 0; r < 4; ++r) sc[(c * 16 + 4 * g + r) * 129 + 16 * nt + l15] = acc[nt][r];
.LBB0_3214:
	s_lshl_b32 s4, s17, 1
	s_and_b32 s18, s4, -16
	s_waitcnt lgkmcnt(0)
	v_or_b32_e32 v126, s18, v150
	v_ashrrev_i32_e32 v127, 31, v126
	v_lshlrev_b64 v[126:127], 12, v[126:127]
	v_lshl_add_u64 v[126:127], v[2:3], 0, v[126:127]
	global_load_dwordx4 v[128:131], v[126:127], off
	global_load_dwordx4 v[132:135], v[4:5], off
	global_load_dwordx4 v[136:139], v[6:7], off
	global_load_dwordx4 v[140:143], v[8:9], off
	global_load_dwordx4 v[144:147], v[10:11], off
	global_load_dwordx4 v[160:163], v[12:13], off
	global_load_dwordx4 v[164:167], v[14:15], off
	global_load_dwordx4 v[168:171], v[16:17], off
	global_load_dwordx4 v[172:175], v[18:19], off
	global_load_dwordx4 v[176:179], v[126:127], off offset:64
	global_load_dwordx4 v[180:183], v[4:5], off offset:64
	global_load_dwordx4 v[184:187], v[20:21], off
	global_load_dwordx4 v[188:191], v[22:23], off
	global_load_dwordx4 v[192:195], v[24:25], off
	global_load_dwordx4 v[196:199], v[26:27], off
	global_load_dwordx4 v[200:203], v[28:29], off
	global_load_dwordx4 v[204:207], v[30:31], off
	global_load_dwordx4 v[208:211], v[32:33], off
	global_load_dwordx4 v[212:215], v[126:127], off offset:128
	global_load_dwordx4 v[216:219], v[4:5], off offset:128
	global_load_dwordx4 v[220:223], v[34:35], off
	global_load_dwordx4 v[224:227], v[36:37], off
	global_load_dwordx4 v[228:231], v[38:39], off
	global_load_dwordx4 v[232:235], v[40:41], off
	global_load_dwordx4 v[236:239], v[42:43], off
	global_load_dwordx4 v[240:243], v[44:45], off
	global_load_dwordx4 v[244:247], v[46:47], off
	s_mov_b32 s4, 0
	v_mov_b32_e32 v148, 0xff800000
	v_mov_b32_e32 v149, 0xff800000
	v_mov_b32_e32 v159, 0xff800000
	s_waitcnt vmcnt(25)
	v_mfma_f32_16x16x32_bf16 v[132:135], v[128:131], v[132:135], 0
	s_waitcnt vmcnt(24)
	v_mfma_f32_16x16x32_bf16 v[136:139], v[128:131], v[136:139], 0
	s_waitcnt vmcnt(23)
	v_mfma_f32_16x16x32_bf16 v[140:143], v[128:131], v[140:143], 0
	s_waitcnt vmcnt(22)
	v_mfma_f32_16x16x32_bf16 v[144:147], v[128:131], v[144:147], 0
	s_waitcnt vmcnt(21)
	v_mfma_f32_16x16x32_bf16 v[160:163], v[128:131], v[160:163], 0
	s_waitcnt vmcnt(20)
	v_mfma_f32_16x16x32_bf16 v[164:167], v[128:131], v[164:167], 0
	s_waitcnt vmcnt(19)
	v_mfma_f32_16x16x32_bf16 v[168:171], v[128:131], v[168:171], 0
	s_waitcnt vmcnt(18)
	v_mfma_f32_16x16x32_bf16 v[128:131], v[128:131], v[172:175], 0
	s_waitcnt vmcnt(16)
	v_mfma_f32_16x16x32_bf16 v[132:135], v[176:179], v[180:183], v[132:135]
	s_waitcnt vmcnt(15)
	v_mfma_f32_16x16x32_bf16 v[136:139], v[176:179], v[184:187], v[136:139]
	s_waitcnt vmcnt(14)
	v_mfma_f32_16x16x32_bf16 v[140:143], v[176:179], v[188:191], v[140:143]
	s_waitcnt vmcnt(13)
	v_mfma_f32_16x16x32_bf16 v[144:147], v[176:179], v[192:195], v[144:147]
	s_waitcnt vmcnt(12)
	v_mfma_f32_16x16x32_bf16 v[160:163], v[176:179], v[196:199], v[160:163]
	s_waitcnt vmcnt(11)
	v_mfma_f32_16x16x32_bf16 v[164:167], v[176:179], v[200:203], v[164:167]
	s_waitcnt vmcnt(10)
	v_mfma_f32_16x16x32_bf16 v[168:171], v[176:179], v[204:207], v[168:171]
	s_waitcnt vmcnt(9)
	v_mfma_f32_16x16x32_bf16 v[128:131], v[176:179], v[208:211], v[128:131]
	global_load_dwordx4 v[176:179], v[126:127], off offset:192
	global_load_dwordx4 v[180:183], v[4:5], off offset:192
	global_load_dwordx4 v[184:187], v[48:49], off
	global_load_dwordx4 v[188:191], v[50:51], off
	global_load_dwordx4 v[192:195], v[52:53], off
	global_load_dwordx4 v[196:199], v[54:55], off
	global_load_dwordx4 v[200:203], v[56:57], off
	global_load_dwordx4 v[204:207], v[58:59], off
	global_load_dwordx4 v[208:211], v[60:61], off
	s_waitcnt vmcnt(16)
	v_mfma_f32_16x16x32_bf16 v[132:135], v[212:215], v[216:219], v[132:135]
	s_waitcnt vmcnt(15)
	v_mfma_f32_16x16x32_bf16 v[136:139], v[212:215], v[220:223], v[136:139]
	s_waitcnt vmcnt(14)
	v_mfma_f32_16x16x32_bf16 v[140:143], v[212:215], v[224:227], v[140:143]
	s_waitcnt vmcnt(13)
	v_mfma_f32_16x16x32_bf16 v[144:147], v[212:215], v[228:231], v[144:147]
	s_waitcnt vmcnt(12)
	v_mfma_f32_16x16x32_bf16 v[160:163], v[212:215], v[232:235], v[160:163]
	s_waitcnt vmcnt(11)
	v_mfma_f32_16x16x32_bf16 v[164:167], v[212:215], v[236:239], v[164:167]
	s_waitcnt vmcnt(10)
	v_mfma_f32_16x16x32_bf16 v[168:171], v[212:215], v[240:243], v[168:171]
	s_waitcnt vmcnt(9)
	v_mfma_f32_16x16x32_bf16 v[128:131], v[212:215], v[244:247], v[128:131]
	s_waitcnt vmcnt(7)
	v_mfma_f32_16x16x32_bf16 v[132:135], v[176:179], v[180:183], v[132:135]
	s_waitcnt vmcnt(6)
	v_mfma_f32_16x16x32_bf16 v[136:139], v[176:179], v[184:187], v[136:139]
	s_waitcnt vmcnt(5)
	v_mfma_f32_16x16x32_bf16 v[140:143], v[176:179], v[188:191], v[140:143]
	s_waitcnt vmcnt(4)
	v_mfma_f32_16x16x32_bf16 v[144:147], v[176:179], v[192:195], v[144:147]
	s_waitcnt vmcnt(3)
	v_mfma_f32_16x16x32_bf16 v[160:163], v[176:179], v[196:199], v[160:163]
	s_waitcnt vmcnt(2)
	v_mfma_f32_16x16x32_bf16 v[164:167], v[176:179], v[200:203], v[164:167]
	s_waitcnt vmcnt(1)
	v_mfma_f32_16x16x32_bf16 v[168:171], v[176:179], v[204:207], v[168:171]
	s_waitcnt vmcnt(0)
; __device__ __forceinline__ void p11_route(Frame& F) {
;     ...
;         for (int c = 0; c < 2; ++c) {
;             f32x4 acc[8];
; #pragma unroll
;             for (int nt = 0; nt < 8; ++nt) acc[nt] = (f32x4){0.f, 0.f, 0.f, 0.f};
; #pragma unroll
;             for (int ks = 0; ks < 4; ++ks) { const gbf16x8 a = *(const gbf16x8*)(QRY + (size_t)(t0 + l15) * 2048 + h * 256 + c * 128 + 32 * ks + 8 * g);
; #pragma unroll
;                 for (int nt = 0; nt < 8; ++nt) acc[nt] = __builtin_amdgcn_mfma_f32_16x16x32_bf16(a, *(const gbf16x8*)(SK + ((size_t)(h * 2 + c) * PNK + 16 * nt + l15) * 128 + 32 * ks + 8 * g), acc[nt], 0, 0, 0); }
; #pragma unroll
;             for (int nt = 0; nt < 8; ++nt)
; #pragma unroll
;                 for (int r = 0; r < 4; ++r) sc[(c * 16 + 4 * g + r) * 129 + 16 * nt + l15] = acc[nt][r];
	v_mfma_f32_16x16x32_bf16 v[128:131], v[176:179], v[208:211], v[128:131]
	s_nop 3
	ds_write2_b32 v151, v132, v136 offset1:16
	ds_write2_b32 v151, v133, v137 offset0:129 offset1:145
	v_add_u32_e32 v132, 0x400, v151
	ds_write2_b32 v132, v134, v138 offset0:2 offset1:18
	ds_write2_b32 v132, v135, v139 offset0:131 offset1:147
	ds_write2_b32 v151, v140, v144 offset0:32 offset1:48
	ds_write2_b32 v151, v141, v145 offset0:161 offset1:177
	ds_write2_b32 v132, v142, v146 offset0:34 offset1:50
	ds_write2_b32 v132, v143, v147 offset0:163 offset1:179
	ds_write2_b32 v151, v160, v164 offset0:64 offset1:80
	ds_write2_b32 v151, v161, v165 offset0:193 offset1:209
	ds_write2_b32 v132, v162, v166 offset0:66 offset1:82
	ds_write2_b32 v132, v163, v167 offset0:195 offset1:211
	ds_write2_b32 v151, v168, v128 offset0:96 offset1:112
	ds_write2_b32 v151, v169, v129 offset0:225 offset1:241
	ds_write2_b32 v132, v170, v130 offset0:98 offset1:114
	ds_write2_b32 v132, v171, v131 offset0:227 offset1:243
	global_load_dwordx4 v[128:131], v[126:127], off offset:256
	global_load_dwordx4 v[132:135], v[62:63], off
	global_load_dwordx4 v[136:139], v[64:65], off
	global_load_dwordx4 v[140:143], v[66:67], off
	global_load_dwordx4 v[144:147], v[68:69], off
	global_load_dwordx4 v[160:163], v[70:71], off
	global_load_dwordx4 v[164:167], v[72:73], off
	global_load_dwordx4 v[168:171], v[74:75], off
	global_load_dwordx4 v[172:175], v[76:77], off
	global_load_dwordx4 v[176:179], v[126:127], off offset:320
	global_load_dwordx4 v[180:183], v[78:79], off
	global_load_dwordx4 v[184:187], v[80:81], off
	global_load_dwordx4 v[188:191], v[82:83], off
	global_load_dwordx4 v[192:195], v[84:85], off
	global_load_dwordx4 v[196:199], v[86:87], off
	global_load_dwordx4 v[200:203], v[88:89], off
	global_load_dwordx4 v[204:207], v[90:91], off
	global_load_dwordx4 v[208:211], v[92:93], off
	global_load_dwordx4 v[212:215], v[126:127], off offset:384
	global_load_dwordx4 v[216:219], v[94:95], off
	global_load_dwordx4 v[220:223], v[96:97], off
	global_load_dwordx4 v[224:227], v[98:99], off
	global_load_dwordx4 v[228:231], v[100:101], off
	global_load_dwordx4 v[232:235], v[102:103], off
	global_load_dwordx4 v[236:239], v[104:105], off
	global_load_dwordx4 v[240:243], v[106:107], off
	global_load_dwordx4 v[244:247], v[108:109], off
	s_waitcnt vmcnt(25)
	v_mfma_f32_16x16x32_bf16 v[132:135], v[128:131], v[132:135], 0
	s_waitcnt vmcnt(24)
	v_mfma_f32_16x16x32_bf16 v[136:139], v[128:131], v[136:139], 0
	s_waitcnt vmcnt(23)
	v_mfma_f32_16x16x32_bf16 v[140:143], v[128:131], v[140:143], 0
	s_waitcnt vmcnt(22)
	v_mfma_f32_16x16x32_bf16 v[144:147], v[128:131], v[144:147], 0
	s_waitcnt vmcnt(21)
	v_mfma_f32_16x16x32_bf16 v[160:163], v[128:131], v[160:163], 0
	s_waitcnt vmcnt(20)
	v_mfma_f32_16x16x32_bf16 v[164:167], v[128:131], v[164:167], 0
	s_waitcnt vmcnt(19)
	v_mfma_f32_16x16x32_bf16 v[168:171], v[128:131], v[168:171], 0
	s_waitcnt vmcnt(18)
	v_mfma_f32_16x16x32_bf16 v[128:131], v[128:131], v[172:175], 0
	s_waitcnt vmcnt(16)
	v_mfma_f32_16x16x32_bf16 v[132:135], v[176:179], v[180:183], v[132:135]
	s_waitcnt vmcnt(15)
	v_mfma_f32_16x16x32_bf16 v[136:139], v[176:179], v[184:187], v[136:139]
	s_waitcnt vmcnt(14)
	v_mfma_f32_16x16x32_bf16 v[140:143], v[176:179], v[188:191], v[140:143]
	s_waitcnt vmcnt(13)
	v_mfma_f32_16x16x32_bf16 v[144:147], v[176:179], v[192:195], v[144:147]
	s_waitcnt vmcnt(12)
	v_mfma_f32_16x16x32_bf16 v[160:163], v[176:179], v[196:199], v[160:163]
	s_waitcnt vmcnt(11)
	v_mfma_f32_16x16x32_bf16 v[164:167], v[176:179], v[200:203], v[164:167]
	s_waitcnt vmcnt(10)
	v_mfma_f32_16x16x32_bf16 v[168:171], v[176:179], v[204:207], v[168:171]
	s_waitcnt vmcnt(9)
	v_mfma_f32_16x16x32_bf16 v[128:131], v[176:179], v[208:211], v[128:131]
	global_load_dwordx4 v[176:179], v[126:127], off offset:448
	global_load_dwordx4 v[180:183], v[110:111], off
	global_load_dwordx4 v[184:187], v[112:113], off
	global_load_dwordx4 v[188:191], v[114:115], off
	global_load_dwordx4 v[192:195], v[116:117], off
	global_load_dwordx4 v[196:199], v[118:119], off
	global_load_dwordx4 v[200:203], v[120:121], off
	global_load_dwordx4 v[204:207], v[122:123], off
	global_load_dwordx4 v[208:211], v[124:125], off
	s_waitcnt vmcnt(16)
	v_mfma_f32_16x16x32_bf16 v[132:135], v[212:215], v[216:219], v[132:135]
	s_waitcnt vmcnt(15)
	v_mfma_f32_16x16x32_bf16 v[136:139], v[212:215], v[220:223], v[136:139]
	s_waitcnt vmcnt(14)
	v_mfma_f32_16x16x32_bf16 v[140:143], v[212:215], v[224:227], v[140:143]
	s_waitcnt vmcnt(13)
	v_mfma_f32_16x16x32_bf16 v[144:147], v[212:215], v[228:231], v[144:147]
	s_waitcnt vmcnt(12)
	v_mfma_f32_16x16x32_bf16 v[160:163], v[212:215], v[232:235], v[160:163]
	s_waitcnt vmcnt(11)
	v_mfma_f32_16x16x32_bf16 v[164:167], v[212:215], v[236:239], v[164:167]
	s_waitcnt vmcnt(10)
	v_mfma_f32_16x16x32_bf16 v[168:171], v[212:215], v[240:243], v[168:171]
	s_waitcnt vmcnt(9)
	v_mfma_f32_16x16x32_bf16 v[128:131], v[212:215], v[244:247], v[128:131]
	s_waitcnt vmcnt(7)
	v_mfma_f32_16x16x32_bf16 v[132:135], v[176:179], v[180:183], v[132:135]
	s_waitcnt vmcnt(6)
	v_mfma_f32_16x16x32_bf16 v[136:139], v[176:179], v[184:187], v[136:139]
	s_waitcnt vmcnt(5)
	v_mfma_f32_16x16x32_bf16 v[140:143], v[176:179], v[188:191], v[140:143]
	s_waitcnt vmcnt(4)
	v_mfma_f32_16x16x32_bf16 v[144:147], v[176:179], v[192:195], v[144:147]
	s_waitcnt vmcnt(3)
	v_mfma_f32_16x16x32_bf16 v[160:163], v[176:179], v[196:199], v[160:163]
	s_waitcnt vmcnt(2)
	v_mfma_f32_16x16x32_bf16 v[164:167], v[176:179], v[200:203], v[164:167]
	s_waitcnt vmcnt(1)
	v_mfma_f32_16x16x32_bf16 v[168:171], v[176:179], v[204:207], v[168:171]
	s_waitcnt vmcnt(0)
; #define LAS __attribute__((address_space(3)))
; __device__ __forceinline__ float uniq_key(float s, int n) { return __uint_as_float((__float_as_uint(s) & ~0xffu) | (unsigned)(255 - n)); }
; #define INS16(A_, X_) do { float x_ = (X_); _Pragma("unroll") for (int i_ = 0; i_ < 16; ++i_) { const float hi_ = fmaxf(A_[i_], x_); x_ = fminf(A_[i_], x_); A_[i_] = hi_; } } while (0)
; __device__ __forceinline__ void p11_route(Frame& F) {
;     ...
;             for (int nt = 0; nt < 8; ++nt)
; #pragma unroll
;                 for (int r = 0; r < 4; ++r) sc[(c * 16 + 4 * g + r) * 129 + 16 * nt + l15] = acc[nt][r];
;         }
;         { LAS float* row = sc + (F.lane & 31) * 129; float a[16]; const int nb = (F.lane >> 5) * (PNK / 2);
; #pragma unroll
;             for (int i = 0; i < 16; ++i) a[i] = -INFINITY;
; #pragma unroll 4
;             for (int n = 0; n < PNK / 2; ++n) INS16(a, uniq_key(row[nb + n], nb + n));
	v_mfma_f32_16x16x32_bf16 v[126:129], v[176:179], v[208:211], v[128:131]
	s_nop 2
	v_add_u32_e32 v130, 0x2000, v151
	v_add_u32_e32 v131, 0x2400, v151
	ds_write2_b32 v130, v132, v136 offset0:16 offset1:32
	ds_write2_b32 v130, v133, v137 offset0:145 offset1:161
	ds_write2_b32 v131, v134, v138 offset0:18 offset1:34
	ds_write2_b32 v131, v135, v139 offset0:147 offset1:163
	ds_write2_b32 v130, v140, v144 offset0:48 offset1:64
	ds_write2_b32 v130, v141, v145 offset0:177 offset1:193
	ds_write2_b32 v131, v142, v146 offset0:50 offset1:66
	ds_write2_b32 v131, v143, v147 offset0:179 offset1:195
	ds_write2_b32 v130, v160, v164 offset0:80 offset1:96
	ds_write2_b32 v130, v161, v165 offset0:209 offset1:225
	ds_write2_b32 v131, v162, v166 offset0:82 offset1:98
	ds_write2_b32 v131, v163, v167 offset0:211 offset1:227
	ds_write2_b32 v130, v168, v126 offset0:112 offset1:128
	v_add_u32_e32 v126, 0x2200, v151
	ds_write2_b32 v126, v169, v127 offset0:113 offset1:129
	ds_write2_b32 v131, v170, v128 offset0:114 offset1:130
	v_add_u32_e32 v126, 0x2600, v151
	ds_write2_b32 v126, v171, v129 offset0:115 offset1:131
	ds_read2_b32 v[222:223], v155 offset0:0 offset1:1
	ds_read2_b32 v[224:225], v155 offset0:2 offset1:3
	ds_read2_b32 v[226:227], v155 offset0:4 offset1:5
	ds_read2_b32 v[228:229], v155 offset0:6 offset1:7
	ds_read2_b32 v[230:231], v155 offset0:8 offset1:9
	ds_read2_b32 v[232:233], v155 offset0:10 offset1:11
	ds_read2_b32 v[234:235], v155 offset0:12 offset1:13
	ds_read2_b32 v[236:237], v155 offset0:14 offset1:15
	s_waitcnt lgkmcnt(0)
	ds_read2_b32 v[238:239], v155 offset0:16 offset1:17
	ds_read2_b32 v[240:241], v155 offset0:18 offset1:19
	ds_read2_b32 v[242:243], v155 offset0:20 offset1:21
	ds_read2_b32 v[244:245], v155 offset0:22 offset1:23
	ds_read2_b32 v[246:247], v155 offset0:24 offset1:25
	ds_read2_b32 v[248:249], v155 offset0:26 offset1:27
	ds_read2_b32 v[250:251], v155 offset0:28 offset1:29
	ds_read2_b32 v[252:253], v155 offset0:30 offset1:31
	v_add_u32_e32 v127, 3, v156
	v_and_or_b32 v222, v222, s14, v127
	v_add_u32_e32 v130, 2, v156
	v_and_or_b32 v223, v223, s14, v130
	v_add_u32_e32 v127, 1, v156
	v_and_or_b32 v224, v224, s14, v127
	v_add_u32_e32 v130, 0, v156
	v_and_or_b32 v225, v225, s14, v130
	v_add_u32_e32 v127, -1, v156
	v_and_or_b32 v226, v226, s14, v127
	v_add_u32_e32 v130, -2, v156
	v_and_or_b32 v227, v227, s14, v130
	v_add_u32_e32 v127, -3, v156
	v_and_or_b32 v228, v228, s14, v127
	v_add_u32_e32 v130, -4, v156
	v_and_or_b32 v229, v229, s14, v130
	v_add_u32_e32 v127, -5, v156
	v_and_or_b32 v230, v230, s14, v127
	v_add_u32_e32 v130, -6, v156
	v_and_or_b32 v231, v231, s14, v130
	v_add_u32_e32 v127, -7, v156
	v_and_or_b32 v232, v232, s14, v127
	v_add_u32_e32 v130, -8, v156
	v_and_or_b32 v233, v233, s14, v130
	v_add_u32_e32 v127, -9, v156
	v_and_or_b32 v234, v234, s14, v127
	v_add_u32_e32 v130, -10, v156
	v_and_or_b32 v235, v235, s14, v130
	v_add_u32_e32 v127, -11, v156
	v_and_or_b32 v236, v236, s14, v127
	v_add_u32_e32 v130, -12, v156
	v_and_or_b32 v237, v237, s14, v130
	v_max_f32_e32 v220, v222, v223
	v_min_f32_e32 v223, v222, v223
	v_max_f32_e32 v222, v224, v225
	v_min_f32_e32 v225, v224, v225
	v_max_f32_e32 v224, v220, v222
	v_min_f32_e32 v222, v220, v222
	v_max_f32_e32 v220, v223, v225
	v_min_f32_e32 v225, v223, v225
	v_max_f32_e32 v223, v220, v222
	v_min_f32_e32 v222, v220, v222
	v_max_f32_e32 v220, v226, v227
	v_min_f32_e32 v227, v226, v227
	v_max_f32_e32 v226, v228, v229
	v_min_f32_e32 v229, v228, v229
	v_max_f32_e32 v228, v220, v226
	v_min_f32_e32 v226, v220, v226
	v_max_f32_e32 v220, v227, v229
	v_min_f32_e32 v229, v227, v229
	v_max_f32_e32 v227, v220, v226
	v_min_f32_e32 v226, v220, v226
	v_max_f32_e32 v220, v224, v228
	v_min_f32_e32 v228, v224, v228
	v_max_f32_e32 v224, v222, v226
	v_min_f32_e32 v226, v222, v226
	v_max_f32_e32 v222, v224, v228
	v_min_f32_e32 v228, v224, v228
	v_max_f32_e32 v224, v223, v227
	v_min_f32_e32 v227, v223, v227
	v_max_f32_e32 v223, v225, v229
	v_min_f32_e32 v229, v225, v229
	v_max_f32_e32 v225, v223, v227
	v_min_f32_e32 v227, v223, v227
	v_max_f32_e32 v223, v224, v222
	v_min_f32_e32 v222, v224, v222
	v_max_f32_e32 v224, v225, v228
	v_min_f32_e32 v228, v225, v228
	v_max_f32_e32 v225, v227, v226
	v_min_f32_e32 v226, v227, v226
	v_max_f32_e32 v227, v230, v231
	v_min_f32_e32 v231, v230, v231
	v_max_f32_e32 v230, v232, v233
	v_min_f32_e32 v233, v232, v233
	v_max_f32_e32 v232, v227, v230
	v_min_f32_e32 v230, v227, v230
	v_max_f32_e32 v227, v231, v233
	v_min_f32_e32 v233, v231, v233
	v_max_f32_e32 v231, v227, v230
	v_min_f32_e32 v230, v227, v230
	v_max_f32_e32 v227, v234, v235
	v_min_f32_e32 v235, v234, v235
	v_max_f32_e32 v234, v236, v237
	v_min_f32_e32 v237, v236, v237
	v_max_f32_e32 v236, v227, v234
	v_min_f32_e32 v234, v227, v234
	v_max_f32_e32 v227, v235, v237
	v_min_f32_e32 v237, v235, v237
	v_max_f32_e32 v235, v227, v234
	v_min_f32_e32 v234, v227, v234
	v_max_f32_e32 v227, v232, v236
	v_min_f32_e32 v236, v232, v236
	v_max_f32_e32 v232, v230, v234
	v_min_f32_e32 v234, v230, v234
	v_max_f32_e32 v230, v232, v236
	v_min_f32_e32 v236, v232, v236
	v_max_f32_e32 v232, v231, v235
	v_min_f32_e32 v235, v231, v235
	v_max_f32_e32 v231, v233, v237
	v_min_f32_e32 v237, v233, v237
	v_max_f32_e32 v233, v231, v235
	v_min_f32_e32 v235, v231, v235
	v_max_f32_e32 v231, v232, v230
	v_min_f32_e32 v230, v232, v230
	v_max_f32_e32 v232, v233, v236
	v_min_f32_e32 v236, v233, v236
	v_max_f32_e32 v233, v235, v234
	v_min_f32_e32 v234, v235, v234
	v_max_f32_e32 v235, v220, v227
	v_min_f32_e32 v227, v220, v227
	v_max_f32_e32 v220, v228, v236
	v_min_f32_e32 v236, v228, v236
	v_max_f32_e32 v228, v220, v227
	v_min_f32_e32 v227, v220, v227
; #define LAS __attribute__((address_space(3)))
; __device__ __forceinline__ float uniq_key(float s, int n) { return __uint_as_float((__float_as_uint(s) & ~0xffu) | (unsigned)(255 - n)); }
; #define INS16(A_, X_) do { float x_ = (X_); _Pragma("unroll") for (int i_ = 0; i_ < 16; ++i_) { const float hi_ = fmaxf(A_[i_], x_); x_ = fminf(A_[i_], x_); A_[i_] = hi_; } } while (0)
; __device__ __forceinline__ void p11_route(Frame& F) {
;     ...
;         { LAS float* row = sc + (F.lane & 31) * 129; float a[16]; const int nb = (F.lane >> 5) * (PNK / 2);
; #pragma unroll
;             for (int i = 0; i < 16; ++i) a[i] = -INFINITY;
; #pragma unroll 4
;             for (int n = 0; n < PNK / 2; ++n) INS16(a, uniq_key(row[nb + n], nb + n));
	v_max_f32_e32 v220, v222, v230
	v_min_f32_e32 v230, v222, v230
	v_max_f32_e32 v222, v226, v234
	v_min_f32_e32 v234, v226, v234
	v_max_f32_e32 v226, v222, v230
	v_min_f32_e32 v230, v222, v230
	v_max_f32_e32 v222, v220, v228
	v_min_f32_e32 v228, v220, v228
	v_max_f32_e32 v220, v226, v227
	v_min_f32_e32 v227, v226, v227
	v_max_f32_e32 v226, v230, v236
	v_min_f32_e32 v236, v230, v236
	v_max_f32_e32 v230, v223, v231
	v_min_f32_e32 v231, v223, v231
	v_max_f32_e32 v223, v225, v233
	v_min_f32_e32 v233, v225, v233
	v_max_f32_e32 v225, v223, v231
	v_min_f32_e32 v231, v223, v231
	v_max_f32_e32 v223, v224, v232
	v_min_f32_e32 v232, v224, v232
	v_max_f32_e32 v224, v229, v237
	v_min_f32_e32 v237, v229, v237
	v_max_f32_e32 v229, v224, v232
	v_min_f32_e32 v232, v224, v232
	v_max_f32_e32 v224, v223, v225
	v_min_f32_e32 v225, v223, v225
	v_max_f32_e32 v223, v229, v231
	v_min_f32_e32 v231, v229, v231
	v_max_f32_e32 v229, v232, v233
	v_min_f32_e32 v233, v232, v233
	v_max_f32_e32 v232, v230, v222
	v_min_f32_e32 v222, v230, v222
	v_max_f32_e32 v230, v224, v228
	v_min_f32_e32 v228, v224, v228
	v_max_f32_e32 v224, v225, v220
	v_min_f32_e32 v220, v225, v220
	v_max_f32_e32 v225, v223, v227
	v_min_f32_e32 v227, v223, v227
	v_max_f32_e32 v223, v231, v226
	v_min_f32_e32 v226, v231, v226
	v_max_f32_e32 v231, v229, v236
	v_min_f32_e32 v236, v229, v236
	v_max_f32_e32 v229, v233, v234
	v_min_f32_e32 v234, v233, v234
	s_waitcnt lgkmcnt(0)
	v_add_u32_e32 v127, -13, v156
	v_and_or_b32 v238, v238, s14, v127
	v_add_u32_e32 v130, -14, v156
	v_and_or_b32 v239, v239, s14, v130
	v_add_u32_e32 v127, -15, v156
	v_and_or_b32 v240, v240, s14, v127
	v_add_u32_e32 v130, -16, v156
	v_and_or_b32 v241, v241, s14, v130
	v_add_u32_e32 v127, 0xffffffef, v156
	v_and_or_b32 v242, v242, s14, v127
	v_add_u32_e32 v130, 0xffffffee, v156
	v_and_or_b32 v243, v243, s14, v130
	v_add_u32_e32 v127, 0xffffffed, v156
	v_and_or_b32 v244, v244, s14, v127
	v_add_u32_e32 v130, 0xffffffec, v156
	v_and_or_b32 v245, v245, s14, v130
	v_add_u32_e32 v127, 0xffffffeb, v156
	v_and_or_b32 v246, v246, s14, v127
	v_add_u32_e32 v130, 0xffffffea, v156
	v_and_or_b32 v247, v247, s14, v130
	v_add_u32_e32 v127, 0xffffffe9, v156
	v_and_or_b32 v248, v248, s14, v127
	v_add_u32_e32 v130, 0xffffffe8, v156
	v_and_or_b32 v249, v249, s14, v130
	v_add_u32_e32 v127, 0xffffffe7, v156
	v_and_or_b32 v250, v250, s14, v127
	v_add_u32_e32 v130, 0xffffffe6, v156
	v_and_or_b32 v251, v251, s14, v130
	v_add_u32_e32 v127, 0xffffffe5, v156
	v_and_or_b32 v252, v252, s14, v127
	v_add_u32_e32 v130, 0xffffffe4, v156
	v_and_or_b32 v253, v253, s14, v130
	v_max_f32_e32 v128, v238, v239
	v_min_f32_e32 v239, v238, v239
	v_max_f32_e32 v238, v240, v241
	v_min_f32_e32 v241, v240, v241
	v_max_f32_e32 v240, v128, v238
	v_min_f32_e32 v238, v128, v238
	v_max_f32_e32 v128, v239, v241
	v_min_f32_e32 v241, v239, v241
	v_max_f32_e32 v239, v128, v238
	v_min_f32_e32 v238, v128, v238
	v_max_f32_e32 v128, v242, v243
	v_min_f32_e32 v243, v242, v243
	v_max_f32_e32 v242, v244, v245
	v_min_f32_e32 v245, v244, v245
	v_max_f32_e32 v244, v128, v242
	v_min_f32_e32 v242, v128, v242
	v_max_f32_e32 v128, v243, v245
	v_min_f32_e32 v245, v243, v245
	v_max_f32_e32 v243, v128, v242
	v_min_f32_e32 v242, v128, v242
	v_max_f32_e32 v128, v240, v244
	v_min_f32_e32 v244, v240, v244
	v_max_f32_e32 v240, v238, v242
	v_min_f32_e32 v242, v238, v242
	v_max_f32_e32 v238, v240, v244
	v_min_f32_e32 v244, v240, v244
	v_max_f32_e32 v240, v239, v243
	v_min_f32_e32 v243, v239, v243
	v_max_f32_e32 v239, v241, v245
	v_min_f32_e32 v245, v241, v245
	v_max_f32_e32 v241, v239, v243
	v_min_f32_e32 v243, v239, v243
	v_max_f32_e32 v239, v240, v238
	v_min_f32_e32 v238, v240, v238
	v_max_f32_e32 v240, v241, v244
	v_min_f32_e32 v244, v241, v244
	v_max_f32_e32 v241, v243, v242
	v_min_f32_e32 v242, v243, v242
	v_max_f32_e32 v243, v246, v247
	v_min_f32_e32 v247, v246, v247
	v_max_f32_e32 v246, v248, v249
	v_min_f32_e32 v249, v248, v249
	v_max_f32_e32 v248, v243, v246
	v_min_f32_e32 v246, v243, v246
	v_max_f32_e32 v243, v247, v249
	v_min_f32_e32 v249, v247, v249
	v_max_f32_e32 v247, v243, v246
	v_min_f32_e32 v246, v243, v246
	v_max_f32_e32 v243, v250, v251
	v_min_f32_e32 v251, v250, v251
	v_max_f32_e32 v250, v252, v253
	v_min_f32_e32 v253, v252, v253
	v_max_f32_e32 v252, v243, v250
	v_min_f32_e32 v250, v243, v250
	v_max_f32_e32 v243, v251, v253
	v_min_f32_e32 v253, v251, v253
	v_max_f32_e32 v251, v243, v250
	v_min_f32_e32 v250, v243, v250
	v_max_f32_e32 v243, v248, v252
	v_min_f32_e32 v252, v248, v252
	v_max_f32_e32 v248, v246, v250
	v_min_f32_e32 v250, v246, v250
	v_max_f32_e32 v246, v248, v252
	v_min_f32_e32 v252, v248, v252
	v_max_f32_e32 v248, v247, v251
	v_min_f32_e32 v251, v247, v251
	v_max_f32_e32 v247, v249, v253
	v_min_f32_e32 v253, v249, v253
	v_max_f32_e32 v249, v247, v251
	v_min_f32_e32 v251, v247, v251
	v_max_f32_e32 v247, v248, v246
	v_min_f32_e32 v246, v248, v246
	v_max_f32_e32 v248, v249, v252
	v_min_f32_e32 v252, v249, v252
	v_max_f32_e32 v249, v251, v250
	v_min_f32_e32 v250, v251, v250
	v_max_f32_e32 v251, v128, v243
	v_min_f32_e32 v243, v128, v243
	v_max_f32_e32 v128, v244, v252
	v_min_f32_e32 v252, v244, v252
	v_max_f32_e32 v244, v128, v243
	v_min_f32_e32 v243, v128, v243
	v_max_f32_e32 v128, v238, v246
	v_min_f32_e32 v246, v238, v246
	v_max_f32_e32 v238, v242, v250
	v_min_f32_e32 v250, v242, v250
	v_max_f32_e32 v242, v238, v246
	v_min_f32_e32 v246, v238, v246
	v_max_f32_e32 v238, v128, v244
	v_min_f32_e32 v244, v128, v244
	v_max_f32_e32 v128, v242, v243
	v_min_f32_e32 v243, v242, v243
	v_max_f32_e32 v242, v246, v252
	v_min_f32_e32 v252, v246, v252
	v_max_f32_e32 v246, v239, v247
; #define LAS __attribute__((address_space(3)))
; __device__ __forceinline__ float uniq_key(float s, int n) { return __uint_as_float((__float_as_uint(s) & ~0xffu) | (unsigned)(255 - n)); }
; #define INS16(A_, X_) do { float x_ = (X_); _Pragma("unroll") for (int i_ = 0; i_ < 16; ++i_) { const float hi_ = fmaxf(A_[i_], x_); x_ = fminf(A_[i_], x_); A_[i_] = hi_; } } while (0)
; __device__ __forceinline__ void p11_route(Frame& F) {
;     ...
;         { LAS float* row = sc + (F.lane & 31) * 129; float a[16]; const int nb = (F.lane >> 5) * (PNK / 2);
; #pragma unroll
;             for (int i = 0; i < 16; ++i) a[i] = -INFINITY;
; #pragma unroll 4
;             for (int n = 0; n < PNK / 2; ++n) INS16(a, uniq_key(row[nb + n], nb + n));
	v_min_f32_e32 v247, v239, v247
	v_max_f32_e32 v239, v241, v249
	v_min_f32_e32 v249, v241, v249
	v_max_f32_e32 v241, v239, v247
	v_min_f32_e32 v247, v239, v247
	v_max_f32_e32 v239, v240, v248
	v_min_f32_e32 v248, v240, v248
	v_max_f32_e32 v240, v245, v253
	v_min_f32_e32 v253, v245, v253
	v_max_f32_e32 v245, v240, v248
	v_min_f32_e32 v248, v240, v248
	v_max_f32_e32 v240, v239, v241
	v_min_f32_e32 v241, v239, v241
	v_max_f32_e32 v239, v245, v247
	v_min_f32_e32 v247, v245, v247
	v_max_f32_e32 v245, v248, v249
	v_min_f32_e32 v249, v248, v249
	v_max_f32_e32 v248, v246, v238
	v_min_f32_e32 v238, v246, v238
	v_max_f32_e32 v246, v240, v244
	v_min_f32_e32 v244, v240, v244
	v_max_f32_e32 v240, v241, v128
	v_min_f32_e32 v128, v241, v128
	v_max_f32_e32 v241, v239, v243
	v_min_f32_e32 v243, v239, v243
	v_max_f32_e32 v239, v247, v242
	v_min_f32_e32 v242, v247, v242
	v_max_f32_e32 v247, v245, v252
	v_min_f32_e32 v252, v245, v252
	v_max_f32_e32 v245, v249, v250
	v_min_f32_e32 v250, v249, v250
	v_max_f32_e32 v235, v235, v253
	v_max_f32_e32 v232, v232, v250
	v_max_f32_e32 v222, v222, v245
	v_max_f32_e32 v230, v230, v252
	v_max_f32_e32 v228, v228, v247
	v_max_f32_e32 v224, v224, v242
	v_max_f32_e32 v220, v220, v239
	v_max_f32_e32 v225, v225, v243
	v_max_f32_e32 v227, v227, v241
	v_max_f32_e32 v223, v223, v128
	v_max_f32_e32 v226, v226, v240
	v_max_f32_e32 v231, v231, v244
	v_max_f32_e32 v236, v236, v246
	v_max_f32_e32 v229, v229, v238
	v_max_f32_e32 v234, v234, v248
	v_max_f32_e32 v237, v237, v251
	ds_read2_b32 v[238:239], v155 offset0:32 offset1:33
	ds_read2_b32 v[240:241], v155 offset0:34 offset1:35
	ds_read2_b32 v[242:243], v155 offset0:36 offset1:37
	ds_read2_b32 v[244:245], v155 offset0:38 offset1:39
	ds_read2_b32 v[246:247], v155 offset0:40 offset1:41
	ds_read2_b32 v[248:249], v155 offset0:42 offset1:43
	ds_read2_b32 v[250:251], v155 offset0:44 offset1:45
	ds_read2_b32 v[252:253], v155 offset0:46 offset1:47
	v_max_f32_e32 v233, v235, v227
	v_min_f32_e32 v227, v235, v227
	v_max_f32_e32 v235, v232, v223
	v_min_f32_e32 v223, v232, v223
	v_max_f32_e32 v232, v222, v226
	v_min_f32_e32 v226, v222, v226
	v_max_f32_e32 v222, v230, v231
	v_min_f32_e32 v231, v230, v231
	v_max_f32_e32 v230, v228, v236
	v_min_f32_e32 v236, v228, v236
	v_max_f32_e32 v228, v224, v229
	v_min_f32_e32 v229, v224, v229
	v_max_f32_e32 v224, v220, v234
	v_min_f32_e32 v234, v220, v234
	v_max_f32_e32 v220, v225, v237
	v_min_f32_e32 v237, v225, v237
	v_max_f32_e32 v225, v233, v230
	v_min_f32_e32 v230, v233, v230
	v_max_f32_e32 v233, v235, v228
	v_min_f32_e32 v228, v235, v228
	v_max_f32_e32 v235, v232, v224
	v_min_f32_e32 v224, v232, v224
	v_max_f32_e32 v232, v222, v220
	v_min_f32_e32 v220, v222, v220
	v_max_f32_e32 v222, v227, v236
	v_min_f32_e32 v236, v227, v236
	v_max_f32_e32 v227, v223, v229
	v_min_f32_e32 v229, v223, v229
	v_max_f32_e32 v223, v226, v234
	v_min_f32_e32 v234, v226, v234
	v_max_f32_e32 v226, v231, v237
	v_min_f32_e32 v237, v231, v237
	v_max_f32_e32 v231, v225, v235
	v_min_f32_e32 v235, v225, v235
	v_max_f32_e32 v225, v233, v232
	v_min_f32_e32 v232, v233, v232
	v_max_f32_e32 v233, v230, v224
	v_min_f32_e32 v224, v230, v224
	v_max_f32_e32 v230, v228, v220
	v_min_f32_e32 v220, v228, v220
	v_max_f32_e32 v228, v222, v223
	v_min_f32_e32 v223, v222, v223
	v_max_f32_e32 v222, v227, v226
	v_min_f32_e32 v226, v227, v226
	v_max_f32_e32 v227, v236, v234
	v_min_f32_e32 v234, v236, v234
	v_max_f32_e32 v236, v229, v237
	v_min_f32_e32 v237, v229, v237
	v_max_f32_e32 v229, v231, v225
	v_min_f32_e32 v225, v231, v225
	v_max_f32_e32 v231, v235, v232
	v_min_f32_e32 v232, v235, v232
	v_max_f32_e32 v235, v233, v230
	v_min_f32_e32 v230, v233, v230
	v_max_f32_e32 v233, v224, v220
	v_min_f32_e32 v220, v224, v220
	v_max_f32_e32 v224, v228, v222
	v_min_f32_e32 v222, v228, v222
	v_max_f32_e32 v228, v223, v226
	v_min_f32_e32 v226, v223, v226
	v_max_f32_e32 v223, v227, v236
	v_min_f32_e32 v236, v227, v236
	v_max_f32_e32 v227, v234, v237
	v_min_f32_e32 v237, v234, v237
	s_waitcnt lgkmcnt(0)
	v_add_u32_e32 v127, 0xffffffe3, v156
	v_and_or_b32 v238, v238, s14, v127
	v_add_u32_e32 v130, 0xffffffe2, v156
	v_and_or_b32 v239, v239, s14, v130
	v_add_u32_e32 v127, 0xffffffe1, v156
	v_and_or_b32 v240, v240, s14, v127
	v_add_u32_e32 v130, 0xffffffe0, v156
	v_and_or_b32 v241, v241, s14, v130
	v_add_u32_e32 v127, 0xffffffdf, v156
	v_and_or_b32 v242, v242, s14, v127
	v_add_u32_e32 v130, 0xffffffde, v156
	v_and_or_b32 v243, v243, s14, v130
	v_add_u32_e32 v127, 0xffffffdd, v156
	v_and_or_b32 v244, v244, s14, v127
	v_add_u32_e32 v130, 0xffffffdc, v156
	v_and_or_b32 v245, v245, s14, v130
	v_add_u32_e32 v127, 0xffffffdb, v156
	v_and_or_b32 v246, v246, s14, v127
	v_add_u32_e32 v130, 0xffffffda, v156
	v_and_or_b32 v247, v247, s14, v130
	v_add_u32_e32 v127, 0xffffffd9, v156
	v_and_or_b32 v248, v248, s14, v127
	v_add_u32_e32 v130, 0xffffffd8, v156
	v_and_or_b32 v249, v249, s14, v130
	v_add_u32_e32 v127, 0xffffffd7, v156
	v_and_or_b32 v250, v250, s14, v127
	v_add_u32_e32 v130, 0xffffffd6, v156
	v_and_or_b32 v251, v251, s14, v130
	v_add_u32_e32 v127, 0xffffffd5, v156
	v_and_or_b32 v252, v252, s14, v127
	v_add_u32_e32 v130, 0xffffffd4, v156
	v_and_or_b32 v253, v253, s14, v130
	v_max_f32_e32 v128, v238, v239
	v_min_f32_e32 v239, v238, v239
	v_max_f32_e32 v238, v240, v241
	v_min_f32_e32 v241, v240, v241
	v_max_f32_e32 v240, v128, v238
	v_min_f32_e32 v238, v128, v238
	v_max_f32_e32 v128, v239, v241
	v_min_f32_e32 v241, v239, v241
	v_max_f32_e32 v239, v128, v238
	v_min_f32_e32 v238, v128, v238
	v_max_f32_e32 v128, v242, v243
	v_min_f32_e32 v243, v242, v243
	v_max_f32_e32 v242, v244, v245
	v_min_f32_e32 v245, v244, v245
; #define LAS __attribute__((address_space(3)))
; __device__ __forceinline__ float uniq_key(float s, int n) { return __uint_as_float((__float_as_uint(s) & ~0xffu) | (unsigned)(255 - n)); }
; #define INS16(A_, X_) do { float x_ = (X_); _Pragma("unroll") for (int i_ = 0; i_ < 16; ++i_) { const float hi_ = fmaxf(A_[i_], x_); x_ = fminf(A_[i_], x_); A_[i_] = hi_; } } while (0)
; __device__ __forceinline__ void p11_route(Frame& F) {
;     ...
;         { LAS float* row = sc + (F.lane & 31) * 129; float a[16]; const int nb = (F.lane >> 5) * (PNK / 2);
; #pragma unroll
;             for (int i = 0; i < 16; ++i) a[i] = -INFINITY;
; #pragma unroll 4
;             for (int n = 0; n < PNK / 2; ++n) INS16(a, uniq_key(row[nb + n], nb + n));
	v_max_f32_e32 v244, v128, v242
	v_min_f32_e32 v242, v128, v242
	v_max_f32_e32 v128, v243, v245
	v_min_f32_e32 v245, v243, v245
	v_max_f32_e32 v243, v128, v242
	v_min_f32_e32 v242, v128, v242
	v_max_f32_e32 v128, v240, v244
	v_min_f32_e32 v244, v240, v244
	v_max_f32_e32 v240, v238, v242
	v_min_f32_e32 v242, v238, v242
	v_max_f32_e32 v238, v240, v244
	v_min_f32_e32 v244, v240, v244
	v_max_f32_e32 v240, v239, v243
	v_min_f32_e32 v243, v239, v243
	v_max_f32_e32 v239, v241, v245
	v_min_f32_e32 v245, v241, v245
	v_max_f32_e32 v241, v239, v243
	v_min_f32_e32 v243, v239, v243
	v_max_f32_e32 v239, v240, v238
	v_min_f32_e32 v238, v240, v238
	v_max_f32_e32 v240, v241, v244
	v_min_f32_e32 v244, v241, v244
	v_max_f32_e32 v241, v243, v242
	v_min_f32_e32 v242, v243, v242
	v_max_f32_e32 v243, v246, v247
	v_min_f32_e32 v247, v246, v247
	v_max_f32_e32 v246, v248, v249
	v_min_f32_e32 v249, v248, v249
	v_max_f32_e32 v248, v243, v246
	v_min_f32_e32 v246, v243, v246
	v_max_f32_e32 v243, v247, v249
	v_min_f32_e32 v249, v247, v249
	v_max_f32_e32 v247, v243, v246
	v_min_f32_e32 v246, v243, v246
	v_max_f32_e32 v243, v250, v251
	v_min_f32_e32 v251, v250, v251
	v_max_f32_e32 v250, v252, v253
	v_min_f32_e32 v253, v252, v253
	v_max_f32_e32 v252, v243, v250
	v_min_f32_e32 v250, v243, v250
	v_max_f32_e32 v243, v251, v253
	v_min_f32_e32 v253, v251, v253
	v_max_f32_e32 v251, v243, v250
	v_min_f32_e32 v250, v243, v250
	v_max_f32_e32 v243, v248, v252
	v_min_f32_e32 v252, v248, v252
	v_max_f32_e32 v248, v246, v250
	v_min_f32_e32 v250, v246, v250
	v_max_f32_e32 v246, v248, v252
	v_min_f32_e32 v252, v248, v252
	v_max_f32_e32 v248, v247, v251
	v_min_f32_e32 v251, v247, v251
	v_max_f32_e32 v247, v249, v253
	v_min_f32_e32 v253, v249, v253
	v_max_f32_e32 v249, v247, v251
	v_min_f32_e32 v251, v247, v251
	v_max_f32_e32 v247, v248, v246
	v_min_f32_e32 v246, v248, v246
	v_max_f32_e32 v248, v249, v252
	v_min_f32_e32 v252, v249, v252
	v_max_f32_e32 v249, v251, v250
	v_min_f32_e32 v250, v251, v250
	v_max_f32_e32 v251, v128, v243
	v_min_f32_e32 v243, v128, v243
	v_max_f32_e32 v128, v244, v252
	v_min_f32_e32 v252, v244, v252
	v_max_f32_e32 v244, v128, v243
	v_min_f32_e32 v243, v128, v243
	v_max_f32_e32 v128, v238, v246
	v_min_f32_e32 v246, v238, v246
	v_max_f32_e32 v238, v242, v250
	v_min_f32_e32 v250, v242, v250
	v_max_f32_e32 v242, v238, v246
	v_min_f32_e32 v246, v238, v246
	v_max_f32_e32 v238, v128, v244
	v_min_f32_e32 v244, v128, v244
	v_max_f32_e32 v128, v242, v243
	v_min_f32_e32 v243, v242, v243
	v_max_f32_e32 v242, v246, v252
	v_min_f32_e32 v252, v246, v252
	v_max_f32_e32 v246, v239, v247
	v_min_f32_e32 v247, v239, v247
	v_max_f32_e32 v239, v241, v249
	v_min_f32_e32 v249, v241, v249
	v_max_f32_e32 v241, v239, v247
	v_min_f32_e32 v247, v239, v247
	v_max_f32_e32 v239, v240, v248
	v_min_f32_e32 v248, v240, v248
	v_max_f32_e32 v240, v245, v253
	v_min_f32_e32 v253, v245, v253
	v_max_f32_e32 v245, v240, v248
	v_min_f32_e32 v248, v240, v248
	v_max_f32_e32 v240, v239, v241
	v_min_f32_e32 v241, v239, v241
	v_max_f32_e32 v239, v245, v247
	v_min_f32_e32 v247, v245, v247
	v_max_f32_e32 v245, v248, v249
	v_min_f32_e32 v249, v248, v249
	v_max_f32_e32 v248, v246, v238
	v_min_f32_e32 v238, v246, v238
	v_max_f32_e32 v246, v240, v244
	v_min_f32_e32 v244, v240, v244
	v_max_f32_e32 v240, v241, v128
	v_min_f32_e32 v128, v241, v128
	v_max_f32_e32 v241, v239, v243
	v_min_f32_e32 v243, v239, v243
	v_max_f32_e32 v239, v247, v242
	v_min_f32_e32 v242, v247, v242
	v_max_f32_e32 v247, v245, v252
	v_min_f32_e32 v252, v245, v252
	v_max_f32_e32 v245, v249, v250
	v_min_f32_e32 v250, v249, v250
	v_max_f32_e32 v229, v229, v253
	v_max_f32_e32 v225, v225, v250
	v_max_f32_e32 v231, v231, v245
	v_max_f32_e32 v232, v232, v252
	v_max_f32_e32 v235, v235, v247
	v_max_f32_e32 v230, v230, v242
	v_max_f32_e32 v233, v233, v239
	v_max_f32_e32 v220, v220, v243
	v_max_f32_e32 v224, v224, v241
	v_max_f32_e32 v222, v222, v128
	v_max_f32_e32 v228, v228, v240
	v_max_f32_e32 v226, v226, v244
	v_max_f32_e32 v223, v223, v246
	v_max_f32_e32 v236, v236, v238
	v_max_f32_e32 v227, v227, v248
	v_max_f32_e32 v237, v237, v251
	ds_read2_b32 v[238:239], v155 offset0:48 offset1:49
	ds_read2_b32 v[240:241], v155 offset0:50 offset1:51
	ds_read2_b32 v[242:243], v155 offset0:52 offset1:53
	ds_read2_b32 v[244:245], v155 offset0:54 offset1:55
	ds_read2_b32 v[246:247], v155 offset0:56 offset1:57
	ds_read2_b32 v[248:249], v155 offset0:58 offset1:59
	ds_read2_b32 v[250:251], v155 offset0:60 offset1:61
	ds_read2_b32 v[252:253], v155 offset0:62 offset1:63
	v_max_f32_e32 v234, v229, v224
	v_min_f32_e32 v224, v229, v224
	v_max_f32_e32 v229, v225, v222
	v_min_f32_e32 v222, v225, v222
	v_max_f32_e32 v225, v231, v228
	v_min_f32_e32 v228, v231, v228
	v_max_f32_e32 v231, v232, v226
	v_min_f32_e32 v226, v232, v226
	v_max_f32_e32 v232, v235, v223
	v_min_f32_e32 v223, v235, v223
	v_max_f32_e32 v235, v230, v236
	v_min_f32_e32 v236, v230, v236
	v_max_f32_e32 v230, v233, v227
	v_min_f32_e32 v227, v233, v227
	v_max_f32_e32 v233, v220, v237
	v_min_f32_e32 v237, v220, v237
	v_max_f32_e32 v220, v234, v232
	v_min_f32_e32 v232, v234, v232
	v_max_f32_e32 v234, v229, v235
	v_min_f32_e32 v235, v229, v235
	v_max_f32_e32 v229, v225, v230
	v_min_f32_e32 v230, v225, v230
	v_max_f32_e32 v225, v231, v233
	v_min_f32_e32 v233, v231, v233
	v_max_f32_e32 v231, v224, v223
	v_min_f32_e32 v223, v224, v223
	v_max_f32_e32 v224, v222, v236
	v_min_f32_e32 v236, v222, v236
	v_max_f32_e32 v222, v228, v227
	v_min_f32_e32 v227, v228, v227
	v_max_f32_e32 v228, v226, v237
	v_min_f32_e32 v237, v226, v237
	v_max_f32_e32 v226, v220, v229
	v_min_f32_e32 v229, v220, v229
	v_max_f32_e32 v220, v234, v225
	v_min_f32_e32 v225, v234, v225
	v_max_f32_e32 v234, v232, v230
	v_min_f32_e32 v230, v232, v230
	v_max_f32_e32 v232, v235, v233
	v_min_f32_e32 v233, v235, v233
	v_max_f32_e32 v235, v231, v222
	v_min_f32_e32 v222, v231, v222
	v_max_f32_e32 v231, v224, v228
	v_min_f32_e32 v228, v224, v228
	v_max_f32_e32 v224, v223, v227
	v_min_f32_e32 v227, v223, v227
	v_max_f32_e32 v223, v236, v237
	v_min_f32_e32 v237, v236, v237
	v_max_f32_e32 v236, v226, v220
	v_min_f32_e32 v220, v226, v220
	v_max_f32_e32 v226, v229, v225
	v_min_f32_e32 v225, v229, v225
	v_max_f32_e32 v229, v234, v232
	v_min_f32_e32 v232, v234, v232
	v_max_f32_e32 v234, v230, v233
	v_min_f32_e32 v233, v230, v233
	v_max_f32_e32 v230, v235, v231
	v_min_f32_e32 v231, v235, v231
	v_max_f32_e32 v235, v222, v228
	v_min_f32_e32 v228, v222, v228
	v_max_f32_e32 v222, v224, v223
	v_min_f32_e32 v223, v224, v223
	v_max_f32_e32 v224, v227, v237
	v_min_f32_e32 v237, v227, v237
	s_waitcnt lgkmcnt(0)
; #define LAS __attribute__((address_space(3)))
; __device__ __forceinline__ float uniq_key(float s, int n) { return __uint_as_float((__float_as_uint(s) & ~0xffu) | (unsigned)(255 - n)); }
; #define INS16(A_, X_) do { float x_ = (X_); _Pragma("unroll") for (int i_ = 0; i_ < 16; ++i_) { const float hi_ = fmaxf(A_[i_], x_); x_ = fminf(A_[i_], x_); A_[i_] = hi_; } } while (0)
; __device__ __forceinline__ void p11_route(Frame& F) {
;     ...
;         { LAS float* row = sc + (F.lane & 31) * 129; float a[16]; const int nb = (F.lane >> 5) * (PNK / 2);
; #pragma unroll
;             for (int i = 0; i < 16; ++i) a[i] = -INFINITY;
; #pragma unroll 4
;             for (int n = 0; n < PNK / 2; ++n) INS16(a, uniq_key(row[nb + n], nb + n));
	v_add_u32_e32 v127, 0xffffffd3, v156
	v_and_or_b32 v238, v238, s14, v127
	v_add_u32_e32 v130, 0xffffffd2, v156
	v_and_or_b32 v239, v239, s14, v130
	v_add_u32_e32 v127, 0xffffffd1, v156
	v_and_or_b32 v240, v240, s14, v127
	v_add_u32_e32 v130, 0xffffffd0, v156
	v_and_or_b32 v241, v241, s14, v130
	v_add_u32_e32 v127, 0xffffffcf, v156
	v_and_or_b32 v242, v242, s14, v127
	v_add_u32_e32 v130, 0xffffffce, v156
	v_and_or_b32 v243, v243, s14, v130
	v_add_u32_e32 v127, 0xffffffcd, v156
	v_and_or_b32 v244, v244, s14, v127
	v_add_u32_e32 v130, 0xffffffcc, v156
	v_and_or_b32 v245, v245, s14, v130
	v_add_u32_e32 v127, 0xffffffcb, v156
	v_and_or_b32 v246, v246, s14, v127
	v_add_u32_e32 v130, 0xffffffca, v156
	v_and_or_b32 v247, v247, s14, v130
	v_add_u32_e32 v127, 0xffffffc9, v156
	v_and_or_b32 v248, v248, s14, v127
	v_add_u32_e32 v130, 0xffffffc8, v156
	v_and_or_b32 v249, v249, s14, v130
	v_add_u32_e32 v127, 0xffffffc7, v156
	v_and_or_b32 v250, v250, s14, v127
	v_add_u32_e32 v130, 0xffffffc6, v156
	v_and_or_b32 v251, v251, s14, v130
	v_add_u32_e32 v127, 0xffffffc5, v156
	v_and_or_b32 v252, v252, s14, v127
	v_add_u32_e32 v130, 0xffffffc4, v156
	v_and_or_b32 v253, v253, s14, v130
	v_max_f32_e32 v128, v238, v239
	v_min_f32_e32 v239, v238, v239
	v_max_f32_e32 v238, v240, v241
	v_min_f32_e32 v241, v240, v241
	v_max_f32_e32 v240, v128, v238
	v_min_f32_e32 v238, v128, v238
	v_max_f32_e32 v128, v239, v241
	v_min_f32_e32 v241, v239, v241
	v_max_f32_e32 v239, v128, v238
	v_min_f32_e32 v238, v128, v238
	v_max_f32_e32 v128, v242, v243
	v_min_f32_e32 v243, v242, v243
	v_max_f32_e32 v242, v244, v245
	v_min_f32_e32 v245, v244, v245
	v_max_f32_e32 v244, v128, v242
	v_min_f32_e32 v242, v128, v242
	v_max_f32_e32 v128, v243, v245
	v_min_f32_e32 v245, v243, v245
	v_max_f32_e32 v243, v128, v242
	v_min_f32_e32 v242, v128, v242
	v_max_f32_e32 v128, v240, v244
	v_min_f32_e32 v244, v240, v244
	v_max_f32_e32 v240, v238, v242
	v_min_f32_e32 v242, v238, v242
	v_max_f32_e32 v238, v240, v244
	v_min_f32_e32 v244, v240, v244
	v_max_f32_e32 v240, v239, v243
	v_min_f32_e32 v243, v239, v243
	v_max_f32_e32 v239, v241, v245
	v_min_f32_e32 v245, v241, v245
	v_max_f32_e32 v241, v239, v243
	v_min_f32_e32 v243, v239, v243
	v_max_f32_e32 v239, v240, v238
	v_min_f32_e32 v238, v240, v238
	v_max_f32_e32 v240, v241, v244
	v_min_f32_e32 v244, v241, v244
	v_max_f32_e32 v241, v243, v242
	v_min_f32_e32 v242, v243, v242
	v_max_f32_e32 v243, v246, v247
	v_min_f32_e32 v247, v246, v247
	v_max_f32_e32 v246, v248, v249
	v_min_f32_e32 v249, v248, v249
	v_max_f32_e32 v248, v243, v246
	v_min_f32_e32 v246, v243, v246
	v_max_f32_e32 v243, v247, v249
	v_min_f32_e32 v249, v247, v249
	v_max_f32_e32 v247, v243, v246
	v_min_f32_e32 v246, v243, v246
	v_max_f32_e32 v243, v250, v251
	v_min_f32_e32 v251, v250, v251
	v_max_f32_e32 v250, v252, v253
	v_min_f32_e32 v253, v252, v253
	v_max_f32_e32 v252, v243, v250
	v_min_f32_e32 v250, v243, v250
	v_max_f32_e32 v243, v251, v253
	v_min_f32_e32 v253, v251, v253
	v_max_f32_e32 v251, v243, v250
	v_min_f32_e32 v250, v243, v250
	v_max_f32_e32 v243, v248, v252
	v_min_f32_e32 v252, v248, v252
	v_max_f32_e32 v248, v246, v250
	v_min_f32_e32 v250, v246, v250
	v_max_f32_e32 v246, v248, v252
	v_min_f32_e32 v252, v248, v252
	v_max_f32_e32 v248, v247, v251
	v_min_f32_e32 v251, v247, v251
	v_max_f32_e32 v247, v249, v253
	v_min_f32_e32 v253, v249, v253
	v_max_f32_e32 v249, v247, v251
	v_min_f32_e32 v251, v247, v251
	v_max_f32_e32 v247, v248, v246
	v_min_f32_e32 v246, v248, v246
	v_max_f32_e32 v248, v249, v252
	v_min_f32_e32 v252, v249, v252
	v_max_f32_e32 v249, v251, v250
	v_min_f32_e32 v250, v251, v250
	v_max_f32_e32 v251, v128, v243
	v_min_f32_e32 v243, v128, v243
	v_max_f32_e32 v128, v244, v252
	v_min_f32_e32 v252, v244, v252
	v_max_f32_e32 v244, v128, v243
	v_min_f32_e32 v243, v128, v243
	v_max_f32_e32 v128, v238, v246
	v_min_f32_e32 v246, v238, v246
	v_max_f32_e32 v238, v242, v250
	v_min_f32_e32 v250, v242, v250
	v_max_f32_e32 v242, v238, v246
	v_min_f32_e32 v246, v238, v246
	v_max_f32_e32 v238, v128, v244
	v_min_f32_e32 v244, v128, v244
	v_max_f32_e32 v128, v242, v243
	v_min_f32_e32 v243, v242, v243
	v_max_f32_e32 v242, v246, v252
	v_min_f32_e32 v252, v246, v252
	v_max_f32_e32 v246, v239, v247
	v_min_f32_e32 v247, v239, v247
	v_max_f32_e32 v239, v241, v249
	v_min_f32_e32 v249, v241, v249
	v_max_f32_e32 v241, v239, v247
	v_min_f32_e32 v247, v239, v247
	v_max_f32_e32 v239, v240, v248
	v_min_f32_e32 v248, v240, v248
	v_max_f32_e32 v240, v245, v253
	v_min_f32_e32 v253, v245, v253
	v_max_f32_e32 v245, v240, v248
	v_min_f32_e32 v248, v240, v248
	v_max_f32_e32 v240, v239, v241
	v_min_f32_e32 v241, v239, v241
	v_max_f32_e32 v239, v245, v247
	v_min_f32_e32 v247, v245, v247
	v_max_f32_e32 v245, v248, v249
	v_min_f32_e32 v249, v248, v249
	v_max_f32_e32 v248, v246, v238
	v_min_f32_e32 v238, v246, v238
	v_max_f32_e32 v246, v240, v244
	v_min_f32_e32 v244, v240, v244
	v_max_f32_e32 v240, v241, v128
	v_min_f32_e32 v128, v241, v128
	v_max_f32_e32 v241, v239, v243
	v_min_f32_e32 v243, v239, v243
	v_max_f32_e32 v239, v247, v242
	v_min_f32_e32 v242, v247, v242
	v_max_f32_e32 v247, v245, v252
	v_min_f32_e32 v252, v245, v252
	v_max_f32_e32 v245, v249, v250
	v_min_f32_e32 v250, v249, v250
	v_max_f32_e32 v236, v236, v253
	v_max_f32_e32 v220, v220, v250
	v_max_f32_e32 v226, v226, v245
	v_max_f32_e32 v225, v225, v252
	v_max_f32_e32 v229, v229, v247
	v_max_f32_e32 v232, v232, v242
	v_max_f32_e32 v234, v234, v239
	v_max_f32_e32 v233, v233, v243
	v_max_f32_e32 v230, v230, v241
	v_max_f32_e32 v231, v231, v128
	v_max_f32_e32 v235, v235, v240
	v_max_f32_e32 v228, v228, v244
	v_max_f32_e32 v222, v222, v246
; __device__ __forceinline__ float uniq_key(float s, int n) { return __uint_as_float((__float_as_uint(s) & ~0xffu) | (unsigned)(255 - n)); }
; #define INS16(A_, X_) do { float x_ = (X_); _Pragma("unroll") for (int i_ = 0; i_ < 16; ++i_) { const float hi_ = fmaxf(A_[i_], x_); x_ = fminf(A_[i_], x_); A_[i_] = hi_; } } while (0)
; __device__ __forceinline__ void p11_route(Frame& F) {
;     ...
;             for (int n = 0; n < PNK / 2; ++n) INS16(a, uniq_key(row[nb + n], nb + n));
;             float o[16];
; #pragma unroll
;             for (int i = 0; i < 16; ++i) o[i] = __builtin_bit_cast(float, __builtin_amdgcn_ds_bpermute(((F.lane + 32) & 63) << 2, __builtin_bit_cast(int, a[i])));
	v_max_f32_e32 v223, v223, v238
	v_max_f32_e32 v224, v224, v248
	v_max_f32_e32 v237, v237, v251
	v_max_f32_e32 v227, v236, v230
	v_min_f32_e32 v230, v236, v230
	v_max_f32_e32 v236, v220, v231
	v_min_f32_e32 v231, v220, v231
	v_max_f32_e32 v220, v226, v235
	v_min_f32_e32 v235, v226, v235
	v_max_f32_e32 v226, v225, v228
	v_min_f32_e32 v228, v225, v228
	v_max_f32_e32 v225, v229, v222
	v_min_f32_e32 v222, v229, v222
	v_max_f32_e32 v229, v232, v223
	v_min_f32_e32 v223, v232, v223
	v_max_f32_e32 v232, v234, v224
	v_min_f32_e32 v224, v234, v224
	v_max_f32_e32 v234, v233, v237
	v_min_f32_e32 v237, v233, v237
	v_max_f32_e32 v233, v227, v225
	v_min_f32_e32 v225, v227, v225
	v_max_f32_e32 v227, v236, v229
	v_min_f32_e32 v229, v236, v229
	v_max_f32_e32 v236, v220, v232
	v_min_f32_e32 v232, v220, v232
	v_max_f32_e32 v220, v226, v234
	v_min_f32_e32 v234, v226, v234
	v_max_f32_e32 v226, v230, v222
	v_min_f32_e32 v222, v230, v222
	v_max_f32_e32 v230, v231, v223
	v_min_f32_e32 v223, v231, v223
	v_max_f32_e32 v231, v235, v224
	v_min_f32_e32 v224, v235, v224
	v_max_f32_e32 v235, v228, v237
	v_min_f32_e32 v237, v228, v237
	v_max_f32_e32 v228, v233, v236
	v_min_f32_e32 v236, v233, v236
	v_max_f32_e32 v233, v227, v220
	v_min_f32_e32 v220, v227, v220
	v_max_f32_e32 v227, v225, v232
	v_min_f32_e32 v232, v225, v232
	v_max_f32_e32 v225, v229, v234
	v_min_f32_e32 v234, v229, v234
	v_max_f32_e32 v229, v226, v231
	v_min_f32_e32 v231, v226, v231
	v_max_f32_e32 v226, v230, v235
	v_min_f32_e32 v235, v230, v235
	v_max_f32_e32 v230, v222, v224
	v_min_f32_e32 v224, v222, v224
	v_max_f32_e32 v222, v223, v237
	v_min_f32_e32 v237, v223, v237
	v_max_f32_e32 v223, v228, v233
	v_min_f32_e32 v233, v228, v233
	v_max_f32_e32 v228, v236, v220
	v_min_f32_e32 v220, v236, v220
	v_max_f32_e32 v236, v227, v225
	v_min_f32_e32 v225, v227, v225
	v_max_f32_e32 v227, v232, v234
	v_min_f32_e32 v234, v232, v234
	v_max_f32_e32 v232, v229, v226
	v_min_f32_e32 v226, v229, v226
	v_max_f32_e32 v229, v231, v235
	v_min_f32_e32 v235, v231, v235
	v_max_f32_e32 v231, v230, v222
	v_min_f32_e32 v222, v230, v222
	v_max_f32_e32 v230, v224, v237
	v_min_f32_e32 v237, v224, v237
	v_mov_b32_e32 v137, v223
	v_mov_b32_e32 v139, v233
	v_mov_b32_e32 v140, v228
	v_mov_b32_e32 v141, v220
	v_mov_b32_e32 v142, v236
	v_mov_b32_e32 v143, v225
	v_mov_b32_e32 v144, v227
	v_mov_b32_e32 v145, v234
	v_mov_b32_e32 v147, v232
	v_mov_b32_e32 v148, v226
	v_mov_b32_e32 v149, v229
	v_mov_b32_e32 v159, v235
	v_mov_b32_e32 v161, v231
	v_mov_b32_e32 v162, v222
	v_mov_b32_e32 v160, v230
	v_mov_b32_e32 v129, v237
	ds_bpermute_b32 v166, v153, v137
	ds_bpermute_b32 v165, v153, v139
	ds_bpermute_b32 v164, v153, v140
	ds_bpermute_b32 v163, v153, v141
	ds_bpermute_b32 v146, v153, v142
	ds_bpermute_b32 v138, v153, v143
	ds_bpermute_b32 v136, v153, v144
	ds_bpermute_b32 v135, v153, v145
	ds_bpermute_b32 v134, v153, v147
	ds_bpermute_b32 v133, v153, v148
	ds_bpermute_b32 v132, v153, v149
	ds_bpermute_b32 v131, v153, v159
	ds_bpermute_b32 v130, v153, v161
	ds_bpermute_b32 v128, v153, v162
	ds_bpermute_b32 v127, v153, v160
	ds_bpermute_b32 v126, v153, v129
	s_and_saveexec_b64 s[4:5], s[0:1]
	s_cbranch_execz .LBB0_3218
; #define INS16(A_, X_) do { float x_ = (X_); _Pragma("unroll") for (int i_ = 0; i_ < 16; ++i_) { const float hi_ = fmaxf(A_[i_], x_); x_ = fminf(A_[i_], x_); A_[i_] = hi_; } } while (0)
; __device__ __forceinline__ void p11_route(Frame& F) {
;     ...
;             for (int i = 0; i < 16; ++i) INS16(a, o[i]);
;           if (F.lane < 32) {
;             float tv[16]; int ti[16];
; #pragma unroll
;             for (int i = 0; i < 16; ++i) { ti[i] = 255 - (int)(__float_as_uint(a[i]) & 255u); tv[i] = row[ti[i]]; }
; #pragma unroll
;             for (int i = 0; i < 16; ++i) { row[i] = tv[i]; row[16 + i] = __int_as_float(ti[i]); }
	s_waitcnt lgkmcnt(0)
	v_max_f32_e32 v222, v137, v126
	v_max_f32_e32 v223, v139, v127
	v_max_f32_e32 v224, v140, v128
	v_max_f32_e32 v225, v141, v130
	v_max_f32_e32 v226, v142, v131
	v_max_f32_e32 v227, v143, v132
	v_max_f32_e32 v228, v144, v133
	v_max_f32_e32 v229, v145, v134
	v_max_f32_e32 v230, v147, v135
	v_max_f32_e32 v231, v148, v136
	v_max_f32_e32 v232, v149, v138
	v_max_f32_e32 v233, v159, v146
	v_max_f32_e32 v234, v161, v163
	v_max_f32_e32 v235, v162, v164
	v_max_f32_e32 v236, v160, v165
	v_max_f32_e32 v237, v129, v166
	v_max_f32_e32 v238, v222, v230
	v_min_f32_e32 v230, v222, v230
	v_max_f32_e32 v222, v223, v231
	v_min_f32_e32 v231, v223, v231
	v_max_f32_e32 v223, v224, v232
	v_min_f32_e32 v232, v224, v232
	v_max_f32_e32 v224, v225, v233
	v_min_f32_e32 v233, v225, v233
	v_max_f32_e32 v225, v226, v234
	v_min_f32_e32 v234, v226, v234
	v_max_f32_e32 v226, v227, v235
	v_min_f32_e32 v235, v227, v235
	v_max_f32_e32 v227, v228, v236
	v_min_f32_e32 v236, v228, v236
	v_max_f32_e32 v228, v229, v237
	v_min_f32_e32 v237, v229, v237
	v_max_f32_e32 v229, v238, v225
	v_min_f32_e32 v225, v238, v225
	v_max_f32_e32 v238, v222, v226
	v_min_f32_e32 v226, v222, v226
	v_max_f32_e32 v222, v223, v227
	v_min_f32_e32 v227, v223, v227
	v_max_f32_e32 v223, v224, v228
	v_min_f32_e32 v228, v224, v228
	v_max_f32_e32 v224, v230, v234
	v_min_f32_e32 v234, v230, v234
	v_max_f32_e32 v230, v231, v235
	v_min_f32_e32 v235, v231, v235
	v_max_f32_e32 v231, v232, v236
	v_min_f32_e32 v236, v232, v236
	v_max_f32_e32 v232, v233, v237
	v_min_f32_e32 v237, v233, v237
	v_max_f32_e32 v233, v229, v222
	v_min_f32_e32 v222, v229, v222
	v_max_f32_e32 v229, v238, v223
	v_min_f32_e32 v223, v238, v223
	v_max_f32_e32 v238, v225, v227
	v_min_f32_e32 v227, v225, v227
	v_max_f32_e32 v225, v226, v228
	v_min_f32_e32 v228, v226, v228
	v_max_f32_e32 v226, v224, v231
	v_min_f32_e32 v231, v224, v231
	v_max_f32_e32 v224, v230, v232
	v_min_f32_e32 v232, v230, v232
	v_max_f32_e32 v230, v234, v236
	v_min_f32_e32 v236, v234, v236
	v_max_f32_e32 v234, v235, v237
	v_min_f32_e32 v237, v235, v237
	v_max_f32_e32 v235, v233, v229
	v_min_f32_e32 v229, v233, v229
	v_max_f32_e32 v233, v222, v223
	v_min_f32_e32 v223, v222, v223
	v_max_f32_e32 v222, v238, v225
	v_min_f32_e32 v225, v238, v225
	v_max_f32_e32 v238, v227, v228
	v_min_f32_e32 v228, v227, v228
	v_max_f32_e32 v227, v226, v224
	v_min_f32_e32 v224, v226, v224
	v_max_f32_e32 v226, v231, v232
	v_min_f32_e32 v232, v231, v232
	v_max_f32_e32 v231, v230, v234
	v_min_f32_e32 v234, v230, v234
	v_max_f32_e32 v230, v236, v237
	v_min_f32_e32 v237, v236, v237
	v_mov_b32_e32 v126, v235
	v_mov_b32_e32 v127, v229
	v_mov_b32_e32 v128, v233
	v_mov_b32_e32 v130, v223
	v_mov_b32_e32 v131, v222
	v_mov_b32_e32 v132, v225
	v_mov_b32_e32 v133, v238
	v_mov_b32_e32 v134, v228
	v_mov_b32_e32 v135, v227
	v_mov_b32_e32 v136, v224
	v_mov_b32_e32 v137, v226
	v_mov_b32_e32 v138, v232
	v_mov_b32_e32 v139, v231
	v_mov_b32_e32 v140, v234
	v_mov_b32_e32 v141, v230
	v_mov_b32_e32 v129, v237
	v_xor_b32_e32 v127, -1, v127
	v_xor_b32_e32 v126, -1, v126
	v_xor_b32_e32 v130, -1, v130
	v_xor_b32_e32 v128, -1, v128
	v_xor_b32_e32 v132, -1, v132
	v_xor_b32_e32 v131, -1, v131
	v_xor_b32_e32 v134, -1, v134
	v_xor_b32_e32 v133, -1, v133
	v_xor_b32_e32 v136, -1, v136
	v_xor_b32_e32 v135, -1, v135
	v_xor_b32_e32 v138, -1, v138
	v_xor_b32_e32 v137, -1, v137
	v_xor_b32_e32 v140, -1, v140
	v_xor_b32_e32 v139, -1, v139
	v_xor_b32_e32 v129, -1, v129
	v_xor_b32_e32 v141, -1, v141
	v_and_b32_e32 v127, 0xff, v127
	v_and_b32_e32 v126, 0xff, v126
	v_and_b32_e32 v130, 0xff, v130
	v_and_b32_e32 v128, 0xff, v128
	v_and_b32_e32 v132, 0xff, v132
	v_and_b32_e32 v131, 0xff, v131
	v_and_b32_e32 v134, 0xff, v134
	v_and_b32_e32 v133, 0xff, v133
	v_and_b32_e32 v136, 0xff, v136
	v_and_b32_e32 v135, 0xff, v135
	v_and_b32_e32 v138, 0xff, v138
	v_and_b32_e32 v137, 0xff, v137
	v_and_b32_e32 v140, 0xff, v140
	v_and_b32_e32 v139, 0xff, v139
	v_and_b32_e32 v129, 0xff, v129
	v_and_b32_e32 v141, 0xff, v141
	v_lshl_add_u32 v142, v126, 2, v152
	v_lshl_add_u32 v143, v127, 2, v152
	v_lshl_add_u32 v144, v128, 2, v152
	v_lshl_add_u32 v145, v130, 2, v152
	v_lshl_add_u32 v146, v131, 2, v152
	v_lshl_add_u32 v147, v132, 2, v152
	v_lshl_add_u32 v148, v133, 2, v152
	v_lshl_add_u32 v149, v134, 2, v152
	v_lshl_add_u32 v159, v135, 2, v152
	v_lshl_add_u32 v160, v136, 2, v152
	v_lshl_add_u32 v161, v137, 2, v152
	v_lshl_add_u32 v162, v138, 2, v152
	v_lshl_add_u32 v163, v139, 2, v152
	v_lshl_add_u32 v164, v140, 2, v152
	v_lshl_add_u32 v165, v141, 2, v152
	v_lshl_add_u32 v166, v129, 2, v152
	ds_read_b32 v142, v142
	ds_read_b32 v143, v143
	ds_read_b32 v144, v144
	ds_read_b32 v145, v145
	ds_read_b32 v146, v146
	ds_read_b32 v147, v147
	ds_read_b32 v148, v148
	ds_read_b32 v149, v149
	ds_read_b32 v159, v159
	ds_read_b32 v160, v160
	ds_read_b32 v161, v161
	ds_read_b32 v162, v162
	ds_read_b32 v163, v163
	ds_read_b32 v164, v164
	ds_read_b32 v165, v165
	ds_read_b32 v166, v166
	s_waitcnt lgkmcnt(14)
	ds_write2_b32 v152, v142, v143 offset1:1
	ds_write2_b32 v152, v126, v127 offset0:16 offset1:17
	s_waitcnt lgkmcnt(14)
	ds_write2_b32 v152, v144, v145 offset0:2 offset1:3
	ds_write2_b32 v152, v128, v130 offset0:18 offset1:19
	s_waitcnt lgkmcnt(14)
	ds_write2_b32 v152, v146, v147 offset0:4 offset1:5
	ds_write2_b32 v152, v131, v132 offset0:20 offset1:21
	s_waitcnt lgkmcnt(14)
	ds_write2_b32 v152, v148, v149 offset0:6 offset1:7
	ds_write2_b32 v152, v133, v134 offset0:22 offset1:23
	s_waitcnt lgkmcnt(14)
	ds_write2_b32 v152, v159, v160 offset0:8 offset1:9
	ds_write2_b32 v152, v135, v136 offset0:24 offset1:25
	s_waitcnt lgkmcnt(14)
	ds_write2_b32 v152, v161, v162 offset0:10 offset1:11
	ds_write2_b32 v152, v137, v138 offset0:26 offset1:27
	s_waitcnt lgkmcnt(14)
	ds_write2_b32 v152, v163, v164 offset0:12 offset1:13
	ds_write2_b32 v152, v139, v140 offset0:28 offset1:29
	s_waitcnt lgkmcnt(14)
	ds_write2_b32 v152, v165, v166 offset0:14 offset1:15
	ds_write2_b32 v152, v141, v129 offset0:30 offset1:31
	s_or_b64 exec, exec, s[4:5]
	s_and_saveexec_b64 s[12:13], s[2:3]
	s_cbranch_execz .LBB0_3213
	s_branch .LBB0_3219

; #define LAS __attribute__((address_space(3)))
; __device__ __forceinline__ float uniq_key(float s, int n) { return __uint_as_float((__float_as_uint(s) & ~0xffu) | (unsigned)(255 - n)); }
; #define INS16(A_, X_) do { float x_ = (X_); _Pragma("unroll") for (int i_ = 0; i_ < 16; ++i_) { const float hi_ = fmaxf(A_[i_], x_); x_ = fminf(A_[i_], x_); A_[i_] = hi_; } } while (0)
; __device__ __forceinline__ void p11_route(Frame& F) {
;     ...
;         if (F.lane < 16) {
;             const LAS float* r0 = sc + F.lane * 129; const LAS float* r1 = sc + (16 + F.lane) * 129;
;             float v0[16], v1[16];
; #pragma unroll
;             for (int i = 0; i < 16; ++i) { v0[i] = r0[i]; v1[i] = r1[i]; }
;             float b[16];
; #pragma unroll
;             for (int i = 0; i < 16; ++i) b[i] = -INFINITY;
;             { int p = 0;
; #pragma unroll
;               for (int i = 0; i < 16; ++i)
; #pragma unroll
;                   for (int j = 0; j < 16; ++j) if ((i + 1) * (j + 1) <= 16) { INS16(b, uniq_key(v0[i] + v1[j], p)); ++p; } }
.LBB0_3219:
	s_waitcnt lgkmcnt(0)
	v_add_u32_e32 v188, 0x2040, v154
	ds_read2_b32 v[126:127], v154 offset0:0 offset1:1
	ds_read2_b32 v[128:129], v154 offset0:2 offset1:3
	ds_read2_b32 v[130:131], v154 offset0:4 offset1:5
	ds_read2_b32 v[132:133], v154 offset0:6 offset1:7
	ds_read2_b32 v[134:135], v154 offset0:8 offset1:9
	ds_read2_b32 v[136:137], v154 offset0:10 offset1:11
	ds_read2_b32 v[138:139], v154 offset0:12 offset1:13
	ds_read2_b32 v[140:141], v154 offset0:14 offset1:15
	ds_read2_b32 v[142:143], v188 offset0:0 offset1:1
	ds_read2_b32 v[144:145], v188 offset0:2 offset1:3
	ds_read2_b32 v[160:161], v188 offset0:4 offset1:5
	ds_read2_b32 v[162:163], v188 offset0:6 offset1:7
	ds_read2_b32 v[164:165], v188 offset0:8 offset1:9
	ds_read2_b32 v[166:167], v188 offset0:10 offset1:11
	ds_read2_b32 v[168:169], v188 offset0:12 offset1:13
	ds_read2_b32 v[170:171], v188 offset0:14 offset1:15
	s_waitcnt lgkmcnt(0)
	v_add_f32_e32 v222, v126, v142
	v_and_b32_e32 v222, 0xffffff00, v222
	v_or_b32_e32 v222, 0xff, v222
	v_add_f32_e32 v223, v126, v143
	v_and_b32_e32 v223, 0xffffff00, v223
	v_or_b32_e32 v223, 0xfe, v223
	v_add_f32_e32 v224, v126, v144
	v_and_b32_e32 v224, 0xffffff00, v224
	v_or_b32_e32 v224, 0xfd, v224
	v_add_f32_e32 v225, v126, v145
	v_and_b32_e32 v225, 0xffffff00, v225
	v_or_b32_e32 v225, 0xfc, v225
	v_add_f32_e32 v226, v126, v160
	v_and_b32_e32 v226, 0xffffff00, v226
	v_or_b32_e32 v226, 0xfb, v226
	v_add_f32_e32 v227, v126, v161
	v_and_b32_e32 v227, 0xffffff00, v227
	v_or_b32_e32 v227, 0xfa, v227
	v_add_f32_e32 v228, v126, v162
	v_and_b32_e32 v228, 0xffffff00, v228
	v_or_b32_e32 v228, 0xf9, v228
	v_add_f32_e32 v229, v126, v163
	v_and_b32_e32 v229, 0xffffff00, v229
	v_or_b32_e32 v229, 0xf8, v229
	v_add_f32_e32 v230, v126, v164
	v_and_b32_e32 v230, 0xffffff00, v230
	v_or_b32_e32 v230, 0xf7, v230
	v_add_f32_e32 v231, v126, v165
	v_and_b32_e32 v231, 0xffffff00, v231
	v_or_b32_e32 v231, 0xf6, v231
	v_add_f32_e32 v232, v126, v166
	v_and_b32_e32 v232, 0xffffff00, v232
	v_or_b32_e32 v232, 0xf5, v232
	v_add_f32_e32 v233, v126, v167
	v_and_b32_e32 v233, 0xffffff00, v233
	v_or_b32_e32 v233, 0xf4, v233
	v_add_f32_e32 v234, v126, v168
	v_and_b32_e32 v234, 0xffffff00, v234
	v_or_b32_e32 v234, 0xf3, v234
	v_add_f32_e32 v235, v126, v169
	v_and_b32_e32 v235, 0xffffff00, v235
	v_or_b32_e32 v235, 0xf2, v235
	v_add_f32_e32 v236, v126, v170
	v_and_b32_e32 v236, 0xffffff00, v236
	v_or_b32_e32 v236, 0xf1, v236
	v_add_f32_e32 v237, v126, v171
	v_and_b32_e32 v237, 0xffffff00, v237
	v_or_b32_e32 v237, 0xf0, v237
	v_max_f32_e32 v238, v222, v223
	v_min_f32_e32 v223, v222, v223
	v_max_f32_e32 v222, v224, v225
	v_min_f32_e32 v225, v224, v225
	v_max_f32_e32 v224, v238, v222
	v_min_f32_e32 v222, v238, v222
	v_max_f32_e32 v238, v223, v225
	v_min_f32_e32 v225, v223, v225
	v_max_f32_e32 v223, v238, v222
	v_min_f32_e32 v222, v238, v222
	v_max_f32_e32 v238, v226, v227
	v_min_f32_e32 v227, v226, v227
	v_max_f32_e32 v226, v228, v229
	v_min_f32_e32 v229, v228, v229
	v_max_f32_e32 v228, v238, v226
	v_min_f32_e32 v226, v238, v226
	v_max_f32_e32 v238, v227, v229
	v_min_f32_e32 v229, v227, v229
	v_max_f32_e32 v227, v238, v226
	v_min_f32_e32 v226, v238, v226
	v_max_f32_e32 v238, v224, v228
	v_min_f32_e32 v228, v224, v228
	v_max_f32_e32 v224, v222, v226
	v_min_f32_e32 v226, v222, v226
	v_max_f32_e32 v222, v224, v228
	v_min_f32_e32 v228, v224, v228
	v_max_f32_e32 v224, v223, v227
	v_min_f32_e32 v227, v223, v227
	v_max_f32_e32 v223, v225, v229
	v_min_f32_e32 v229, v225, v229
	v_max_f32_e32 v225, v223, v227
	v_min_f32_e32 v227, v223, v227
	v_max_f32_e32 v223, v224, v222
	v_min_f32_e32 v222, v224, v222
	v_max_f32_e32 v224, v225, v228
	v_min_f32_e32 v228, v225, v228
	v_max_f32_e32 v225, v227, v226
	v_min_f32_e32 v226, v227, v226
	v_max_f32_e32 v227, v230, v231
	v_min_f32_e32 v231, v230, v231
	v_max_f32_e32 v230, v232, v233
	v_min_f32_e32 v233, v232, v233
	v_max_f32_e32 v232, v227, v230
	v_min_f32_e32 v230, v227, v230
	v_max_f32_e32 v227, v231, v233
	v_min_f32_e32 v233, v231, v233
	v_max_f32_e32 v231, v227, v230
	v_min_f32_e32 v230, v227, v230
	v_max_f32_e32 v227, v234, v235
	v_min_f32_e32 v235, v234, v235
	v_max_f32_e32 v234, v236, v237
	v_min_f32_e32 v237, v236, v237
	v_max_f32_e32 v236, v227, v234
	v_min_f32_e32 v234, v227, v234
	v_max_f32_e32 v227, v235, v237
	v_min_f32_e32 v237, v235, v237
	v_max_f32_e32 v235, v227, v234
	v_min_f32_e32 v234, v227, v234
	v_max_f32_e32 v227, v232, v236
	v_min_f32_e32 v236, v232, v236
	v_max_f32_e32 v232, v230, v234
	v_min_f32_e32 v234, v230, v234
	v_max_f32_e32 v230, v232, v236
	v_min_f32_e32 v236, v232, v236
	v_max_f32_e32 v232, v231, v235
	v_min_f32_e32 v235, v231, v235
	v_max_f32_e32 v231, v233, v237
	v_min_f32_e32 v237, v233, v237
	v_max_f32_e32 v233, v231, v235
	v_min_f32_e32 v235, v231, v235
	v_max_f32_e32 v231, v232, v230
	v_min_f32_e32 v230, v232, v230
	v_max_f32_e32 v232, v233, v236
	v_min_f32_e32 v236, v233, v236
	v_max_f32_e32 v233, v235, v234
	v_min_f32_e32 v234, v235, v234
	v_max_f32_e32 v235, v238, v227
	v_min_f32_e32 v227, v238, v227
	v_max_f32_e32 v238, v228, v236
	v_min_f32_e32 v236, v228, v236
	v_max_f32_e32 v228, v238, v227
	v_min_f32_e32 v227, v238, v227
	v_max_f32_e32 v238, v222, v230
	v_min_f32_e32 v230, v222, v230
	v_max_f32_e32 v222, v226, v234
	v_min_f32_e32 v234, v226, v234
	v_max_f32_e32 v226, v222, v230
	v_min_f32_e32 v230, v222, v230
	v_max_f32_e32 v222, v238, v228
	v_min_f32_e32 v228, v238, v228
	v_max_f32_e32 v238, v226, v227
	v_min_f32_e32 v227, v226, v227
	v_max_f32_e32 v226, v230, v236
	v_min_f32_e32 v236, v230, v236
	v_max_f32_e32 v230, v223, v231
	v_min_f32_e32 v231, v223, v231
	v_max_f32_e32 v223, v225, v233
; __device__ __forceinline__ float uniq_key(float s, int n) { return __uint_as_float((__float_as_uint(s) & ~0xffu) | (unsigned)(255 - n)); }
; #define INS16(A_, X_) do { float x_ = (X_); _Pragma("unroll") for (int i_ = 0; i_ < 16; ++i_) { const float hi_ = fmaxf(A_[i_], x_); x_ = fminf(A_[i_], x_); A_[i_] = hi_; } } while (0)
; __device__ __forceinline__ void p11_route(Frame& F) {
;     ...
;             { int p = 0;
; #pragma unroll
;               for (int i = 0; i < 16; ++i)
; #pragma unroll
;                   for (int j = 0; j < 16; ++j) if ((i + 1) * (j + 1) <= 16) { INS16(b, uniq_key(v0[i] + v1[j], p)); ++p; } }
	v_min_f32_e32 v233, v225, v233
	v_max_f32_e32 v225, v223, v231
	v_min_f32_e32 v231, v223, v231
	v_max_f32_e32 v223, v224, v232
	v_min_f32_e32 v232, v224, v232
	v_max_f32_e32 v224, v229, v237
	v_min_f32_e32 v237, v229, v237
	v_max_f32_e32 v229, v224, v232
	v_min_f32_e32 v232, v224, v232
	v_max_f32_e32 v224, v223, v225
	v_min_f32_e32 v225, v223, v225
	v_max_f32_e32 v223, v229, v231
	v_min_f32_e32 v231, v229, v231
	v_max_f32_e32 v229, v232, v233
	v_min_f32_e32 v233, v232, v233
	v_max_f32_e32 v232, v230, v222
	v_min_f32_e32 v222, v230, v222
	v_max_f32_e32 v230, v224, v228
	v_min_f32_e32 v228, v224, v228
	v_max_f32_e32 v224, v225, v238
	v_min_f32_e32 v238, v225, v238
	v_max_f32_e32 v225, v223, v227
	v_min_f32_e32 v227, v223, v227
	v_max_f32_e32 v223, v231, v226
	v_min_f32_e32 v226, v231, v226
	v_max_f32_e32 v231, v229, v236
	v_min_f32_e32 v236, v229, v236
	v_max_f32_e32 v229, v233, v234
	v_min_f32_e32 v234, v233, v234
	v_add_f32_e32 v149, v127, v142
	v_and_b32_e32 v149, 0xffffff00, v149
	v_or_b32_e32 v149, 0xef, v149
	v_add_f32_e32 v172, v127, v143
	v_and_b32_e32 v172, 0xffffff00, v172
	v_or_b32_e32 v172, 0xee, v172
	v_add_f32_e32 v173, v127, v144
	v_and_b32_e32 v173, 0xffffff00, v173
	v_or_b32_e32 v173, 0xed, v173
	v_add_f32_e32 v174, v127, v145
	v_and_b32_e32 v174, 0xffffff00, v174
	v_or_b32_e32 v174, 0xec, v174
	v_add_f32_e32 v175, v127, v160
	v_and_b32_e32 v175, 0xffffff00, v175
	v_or_b32_e32 v175, 0xeb, v175
	v_add_f32_e32 v176, v127, v161
	v_and_b32_e32 v176, 0xffffff00, v176
	v_or_b32_e32 v176, 0xea, v176
	v_add_f32_e32 v177, v127, v162
	v_and_b32_e32 v177, 0xffffff00, v177
	v_or_b32_e32 v177, 0xe9, v177
	v_add_f32_e32 v178, v127, v163
	v_and_b32_e32 v178, 0xffffff00, v178
	v_or_b32_e32 v178, 0xe8, v178
	v_add_f32_e32 v179, v128, v142
	v_and_b32_e32 v179, 0xffffff00, v179
	v_or_b32_e32 v179, 0xe7, v179
	v_add_f32_e32 v180, v128, v143
	v_and_b32_e32 v180, 0xffffff00, v180
	v_or_b32_e32 v180, 0xe6, v180
	v_add_f32_e32 v181, v128, v144
	v_and_b32_e32 v181, 0xffffff00, v181
	v_or_b32_e32 v181, 0xe5, v181
	v_add_f32_e32 v182, v128, v145
	v_and_b32_e32 v182, 0xffffff00, v182
	v_or_b32_e32 v182, 0xe4, v182
	v_add_f32_e32 v183, v128, v160
	v_and_b32_e32 v183, 0xffffff00, v183
	v_or_b32_e32 v183, 0xe3, v183
	v_add_f32_e32 v184, v129, v142
	v_and_b32_e32 v184, 0xffffff00, v184
	v_or_b32_e32 v184, 0xe2, v184
	v_add_f32_e32 v185, v129, v143
	v_and_b32_e32 v185, 0xffffff00, v185
	v_or_b32_e32 v185, 0xe1, v185
	v_add_f32_e32 v186, v129, v144
	v_and_b32_e32 v186, 0xffffff00, v186
	v_or_b32_e32 v186, 0xe0, v186
	v_max_f32_e32 v187, v149, v172
	v_min_f32_e32 v172, v149, v172
	v_max_f32_e32 v149, v173, v174
	v_min_f32_e32 v174, v173, v174
	v_max_f32_e32 v173, v187, v149
	v_min_f32_e32 v149, v187, v149
	v_max_f32_e32 v187, v172, v174
	v_min_f32_e32 v174, v172, v174
	v_max_f32_e32 v172, v187, v149
	v_min_f32_e32 v149, v187, v149
	v_max_f32_e32 v187, v175, v176
	v_min_f32_e32 v176, v175, v176
	v_max_f32_e32 v175, v177, v178
	v_min_f32_e32 v178, v177, v178
	v_max_f32_e32 v177, v187, v175
	v_min_f32_e32 v175, v187, v175
	v_max_f32_e32 v187, v176, v178
	v_min_f32_e32 v178, v176, v178
	v_max_f32_e32 v176, v187, v175
	v_min_f32_e32 v175, v187, v175
	v_max_f32_e32 v187, v173, v177
	v_min_f32_e32 v177, v173, v177
	v_max_f32_e32 v173, v149, v175
	v_min_f32_e32 v175, v149, v175
	v_max_f32_e32 v149, v173, v177
	v_min_f32_e32 v177, v173, v177
	v_max_f32_e32 v173, v172, v176
	v_min_f32_e32 v176, v172, v176
	v_max_f32_e32 v172, v174, v178
	v_min_f32_e32 v178, v174, v178
	v_max_f32_e32 v174, v172, v176
	v_min_f32_e32 v176, v172, v176
	v_max_f32_e32 v172, v173, v149
	v_min_f32_e32 v149, v173, v149
	v_max_f32_e32 v173, v174, v177
	v_min_f32_e32 v177, v174, v177
	v_max_f32_e32 v174, v176, v175
	v_min_f32_e32 v175, v176, v175
	v_max_f32_e32 v176, v179, v180
	v_min_f32_e32 v180, v179, v180
	v_max_f32_e32 v179, v181, v182
	v_min_f32_e32 v182, v181, v182
	v_max_f32_e32 v181, v176, v179
	v_min_f32_e32 v179, v176, v179
	v_max_f32_e32 v176, v180, v182
	v_min_f32_e32 v182, v180, v182
	v_max_f32_e32 v180, v176, v179
	v_min_f32_e32 v179, v176, v179
	v_max_f32_e32 v176, v183, v184
	v_min_f32_e32 v184, v183, v184
	v_max_f32_e32 v183, v185, v186
	v_min_f32_e32 v186, v185, v186
	v_max_f32_e32 v185, v176, v183
	v_min_f32_e32 v183, v176, v183
	v_max_f32_e32 v176, v184, v186
	v_min_f32_e32 v186, v184, v186
	v_max_f32_e32 v184, v176, v183
	v_min_f32_e32 v183, v176, v183
	v_max_f32_e32 v176, v181, v185
	v_min_f32_e32 v185, v181, v185
	v_max_f32_e32 v181, v179, v183
	v_min_f32_e32 v183, v179, v183
	v_max_f32_e32 v179, v181, v185
	v_min_f32_e32 v185, v181, v185
	v_max_f32_e32 v181, v180, v184
	v_min_f32_e32 v184, v180, v184
	v_max_f32_e32 v180, v182, v186
	v_min_f32_e32 v186, v182, v186
	v_max_f32_e32 v182, v180, v184
	v_min_f32_e32 v184, v180, v184
	v_max_f32_e32 v180, v181, v179
	v_min_f32_e32 v179, v181, v179
	v_max_f32_e32 v181, v182, v185
	v_min_f32_e32 v185, v182, v185
	v_max_f32_e32 v182, v184, v183
	v_min_f32_e32 v183, v184, v183
	v_max_f32_e32 v184, v187, v176
	v_min_f32_e32 v176, v187, v176
	v_max_f32_e32 v187, v177, v185
	v_min_f32_e32 v185, v177, v185
	v_max_f32_e32 v177, v187, v176
	v_min_f32_e32 v176, v187, v176
	v_max_f32_e32 v187, v149, v179
	v_min_f32_e32 v179, v149, v179
	v_max_f32_e32 v149, v175, v183
	v_min_f32_e32 v183, v175, v183
	v_max_f32_e32 v175, v149, v179
	v_min_f32_e32 v179, v149, v179
	v_max_f32_e32 v149, v187, v177
	v_min_f32_e32 v177, v187, v177
	v_max_f32_e32 v187, v175, v176
	v_min_f32_e32 v176, v175, v176
	v_max_f32_e32 v175, v179, v185
	v_min_f32_e32 v185, v179, v185
	v_max_f32_e32 v179, v172, v180
	v_min_f32_e32 v180, v172, v180
	v_max_f32_e32 v172, v174, v182
; __device__ __forceinline__ float uniq_key(float s, int n) { return __uint_as_float((__float_as_uint(s) & ~0xffu) | (unsigned)(255 - n)); }
; #define INS16(A_, X_) do { float x_ = (X_); _Pragma("unroll") for (int i_ = 0; i_ < 16; ++i_) { const float hi_ = fmaxf(A_[i_], x_); x_ = fminf(A_[i_], x_); A_[i_] = hi_; } } while (0)
; __device__ __forceinline__ void p11_route(Frame& F) {
;     ...
;             { int p = 0;
; #pragma unroll
;               for (int i = 0; i < 16; ++i)
; #pragma unroll
;                   for (int j = 0; j < 16; ++j) if ((i + 1) * (j + 1) <= 16) { INS16(b, uniq_key(v0[i] + v1[j], p)); ++p; } }
	v_min_f32_e32 v182, v174, v182
	v_max_f32_e32 v174, v172, v180
	v_min_f32_e32 v180, v172, v180
	v_max_f32_e32 v172, v173, v181
	v_min_f32_e32 v181, v173, v181
	v_max_f32_e32 v173, v178, v186
	v_min_f32_e32 v186, v178, v186
	v_max_f32_e32 v178, v173, v181
	v_min_f32_e32 v181, v173, v181
	v_max_f32_e32 v173, v172, v174
	v_min_f32_e32 v174, v172, v174
	v_max_f32_e32 v172, v178, v180
	v_min_f32_e32 v180, v178, v180
	v_max_f32_e32 v178, v181, v182
	v_min_f32_e32 v182, v181, v182
	v_max_f32_e32 v181, v179, v149
	v_min_f32_e32 v149, v179, v149
	v_max_f32_e32 v179, v173, v177
	v_min_f32_e32 v177, v173, v177
	v_max_f32_e32 v173, v174, v187
	v_min_f32_e32 v187, v174, v187
	v_max_f32_e32 v174, v172, v176
	v_min_f32_e32 v176, v172, v176
	v_max_f32_e32 v172, v180, v175
	v_min_f32_e32 v175, v180, v175
	v_max_f32_e32 v180, v178, v185
	v_min_f32_e32 v185, v178, v185
	v_max_f32_e32 v178, v182, v183
	v_min_f32_e32 v183, v182, v183
	v_max_f32_e32 v235, v235, v186
	v_max_f32_e32 v232, v232, v183
	v_max_f32_e32 v222, v222, v178
	v_max_f32_e32 v230, v230, v185
	v_max_f32_e32 v228, v228, v180
	v_max_f32_e32 v224, v224, v175
	v_max_f32_e32 v238, v238, v172
	v_max_f32_e32 v225, v225, v176
	v_max_f32_e32 v227, v227, v174
	v_max_f32_e32 v223, v223, v187
	v_max_f32_e32 v226, v226, v173
	v_max_f32_e32 v231, v231, v177
	v_max_f32_e32 v236, v236, v179
	v_max_f32_e32 v229, v229, v149
	v_max_f32_e32 v234, v234, v181
	v_max_f32_e32 v237, v237, v184
	v_max_f32_e32 v233, v235, v227
	v_min_f32_e32 v227, v235, v227
	v_max_f32_e32 v235, v232, v223
	v_min_f32_e32 v223, v232, v223
	v_max_f32_e32 v232, v222, v226
	v_min_f32_e32 v226, v222, v226
	v_max_f32_e32 v222, v230, v231
	v_min_f32_e32 v231, v230, v231
	v_max_f32_e32 v230, v228, v236
	v_min_f32_e32 v236, v228, v236
	v_max_f32_e32 v228, v224, v229
	v_min_f32_e32 v229, v224, v229
	v_max_f32_e32 v224, v238, v234
	v_min_f32_e32 v234, v238, v234
	v_max_f32_e32 v238, v225, v237
	v_min_f32_e32 v237, v225, v237
	v_max_f32_e32 v225, v233, v230
	v_min_f32_e32 v230, v233, v230
	v_max_f32_e32 v233, v235, v228
	v_min_f32_e32 v228, v235, v228
	v_max_f32_e32 v235, v232, v224
	v_min_f32_e32 v224, v232, v224
	v_max_f32_e32 v232, v222, v238
	v_min_f32_e32 v238, v222, v238
	v_max_f32_e32 v222, v227, v236
	v_min_f32_e32 v236, v227, v236
	v_max_f32_e32 v227, v223, v229
	v_min_f32_e32 v229, v223, v229
	v_max_f32_e32 v223, v226, v234
	v_min_f32_e32 v234, v226, v234
	v_max_f32_e32 v226, v231, v237
	v_min_f32_e32 v237, v231, v237
	v_max_f32_e32 v231, v225, v235
	v_min_f32_e32 v235, v225, v235
	v_max_f32_e32 v225, v233, v232
	v_min_f32_e32 v232, v233, v232
	v_max_f32_e32 v233, v230, v224
	v_min_f32_e32 v224, v230, v224
	v_max_f32_e32 v230, v228, v238
	v_min_f32_e32 v238, v228, v238
	v_max_f32_e32 v228, v222, v223
	v_min_f32_e32 v223, v222, v223
	v_max_f32_e32 v222, v227, v226
	v_min_f32_e32 v226, v227, v226
	v_max_f32_e32 v227, v236, v234
	v_min_f32_e32 v234, v236, v234
	v_max_f32_e32 v236, v229, v237
	v_min_f32_e32 v237, v229, v237
	v_max_f32_e32 v229, v231, v225
	v_min_f32_e32 v225, v231, v225
	v_max_f32_e32 v231, v235, v232
	v_min_f32_e32 v232, v235, v232
	v_max_f32_e32 v235, v233, v230
	v_min_f32_e32 v230, v233, v230
	v_max_f32_e32 v233, v224, v238
	v_min_f32_e32 v238, v224, v238
	v_max_f32_e32 v224, v228, v222
	v_min_f32_e32 v222, v228, v222
	v_max_f32_e32 v228, v223, v226
	v_min_f32_e32 v226, v223, v226
	v_max_f32_e32 v223, v227, v236
	v_min_f32_e32 v236, v227, v236
	v_max_f32_e32 v227, v234, v237
	v_min_f32_e32 v237, v234, v237
	v_add_f32_e32 v149, v129, v145
	v_and_b32_e32 v149, 0xffffff00, v149
	v_or_b32_e32 v149, 0xdf, v149
	v_add_f32_e32 v172, v130, v142
	v_and_b32_e32 v172, 0xffffff00, v172
	v_or_b32_e32 v172, 0xde, v172
	v_add_f32_e32 v173, v130, v143
	v_and_b32_e32 v173, 0xffffff00, v173
	v_or_b32_e32 v173, 0xdd, v173
	v_add_f32_e32 v174, v130, v144
	v_and_b32_e32 v174, 0xffffff00, v174
	v_or_b32_e32 v174, 0xdc, v174
	v_add_f32_e32 v175, v131, v142
	v_and_b32_e32 v175, 0xffffff00, v175
	v_or_b32_e32 v175, 0xdb, v175
	v_add_f32_e32 v176, v131, v143
	v_and_b32_e32 v176, 0xffffff00, v176
	v_or_b32_e32 v176, 0xda, v176
	v_add_f32_e32 v177, v132, v142
	v_and_b32_e32 v177, 0xffffff00, v177
	v_or_b32_e32 v177, 0xd9, v177
	v_add_f32_e32 v178, v132, v143
	v_and_b32_e32 v178, 0xffffff00, v178
	v_or_b32_e32 v178, 0xd8, v178
	v_add_f32_e32 v179, v133, v142
	v_and_b32_e32 v179, 0xffffff00, v179
	v_or_b32_e32 v179, 0xd7, v179
	v_add_f32_e32 v180, v133, v143
	v_and_b32_e32 v180, 0xffffff00, v180
	v_or_b32_e32 v180, 0xd6, v180
	v_add_f32_e32 v181, v134, v142
	v_and_b32_e32 v181, 0xffffff00, v181
	v_or_b32_e32 v181, 0xd5, v181
	v_add_f32_e32 v182, v135, v142
	v_and_b32_e32 v182, 0xffffff00, v182
	v_or_b32_e32 v182, 0xd4, v182
	v_add_f32_e32 v183, v136, v142
	v_and_b32_e32 v183, 0xffffff00, v183
	v_or_b32_e32 v183, 0xd3, v183
	v_add_f32_e32 v184, v137, v142
	v_and_b32_e32 v184, 0xffffff00, v184
	v_or_b32_e32 v184, 0xd2, v184
	v_add_f32_e32 v185, v138, v142
	v_and_b32_e32 v185, 0xffffff00, v185
	v_or_b32_e32 v185, 0xd1, v185
	v_add_f32_e32 v186, v139, v142
	v_and_b32_e32 v186, 0xffffff00, v186
	v_or_b32_e32 v186, 0xd0, v186
	v_max_f32_e32 v187, v149, v172
	v_min_f32_e32 v172, v149, v172
	v_max_f32_e32 v149, v173, v174
	v_min_f32_e32 v174, v173, v174
	v_max_f32_e32 v173, v187, v149
	v_min_f32_e32 v149, v187, v149
	v_max_f32_e32 v187, v172, v174
	v_min_f32_e32 v174, v172, v174
	v_max_f32_e32 v172, v187, v149
	v_min_f32_e32 v149, v187, v149
	v_max_f32_e32 v187, v175, v176
	v_min_f32_e32 v176, v175, v176
	v_max_f32_e32 v175, v177, v178
	v_min_f32_e32 v178, v177, v178
	v_max_f32_e32 v177, v187, v175
	v_min_f32_e32 v175, v187, v175
	v_max_f32_e32 v187, v176, v178
; __device__ __forceinline__ float uniq_key(float s, int n) { return __uint_as_float((__float_as_uint(s) & ~0xffu) | (unsigned)(255 - n)); }
; #define INS16(A_, X_) do { float x_ = (X_); _Pragma("unroll") for (int i_ = 0; i_ < 16; ++i_) { const float hi_ = fmaxf(A_[i_], x_); x_ = fminf(A_[i_], x_); A_[i_] = hi_; } } while (0)
; __device__ __forceinline__ void p11_route(Frame& F) {
;     ...
;             { int p = 0;
; #pragma unroll
;               for (int i = 0; i < 16; ++i)
; #pragma unroll
;                   for (int j = 0; j < 16; ++j) if ((i + 1) * (j + 1) <= 16) { INS16(b, uniq_key(v0[i] + v1[j], p)); ++p; } }
	v_min_f32_e32 v178, v176, v178
	v_max_f32_e32 v176, v187, v175
	v_min_f32_e32 v175, v187, v175
	v_max_f32_e32 v187, v173, v177
	v_min_f32_e32 v177, v173, v177
	v_max_f32_e32 v173, v149, v175
	v_min_f32_e32 v175, v149, v175
	v_max_f32_e32 v149, v173, v177
	v_min_f32_e32 v177, v173, v177
	v_max_f32_e32 v173, v172, v176
	v_min_f32_e32 v176, v172, v176
	v_max_f32_e32 v172, v174, v178
	v_min_f32_e32 v178, v174, v178
	v_max_f32_e32 v174, v172, v176
	v_min_f32_e32 v176, v172, v176
	v_max_f32_e32 v172, v173, v149
	v_min_f32_e32 v149, v173, v149
	v_max_f32_e32 v173, v174, v177
	v_min_f32_e32 v177, v174, v177
	v_max_f32_e32 v174, v176, v175
	v_min_f32_e32 v175, v176, v175
	v_max_f32_e32 v176, v179, v180
	v_min_f32_e32 v180, v179, v180
	v_max_f32_e32 v179, v181, v182
	v_min_f32_e32 v182, v181, v182
	v_max_f32_e32 v181, v176, v179
	v_min_f32_e32 v179, v176, v179
	v_max_f32_e32 v176, v180, v182
	v_min_f32_e32 v182, v180, v182
	v_max_f32_e32 v180, v176, v179
	v_min_f32_e32 v179, v176, v179
	v_max_f32_e32 v176, v183, v184
	v_min_f32_e32 v184, v183, v184
	v_max_f32_e32 v183, v185, v186
	v_min_f32_e32 v186, v185, v186
	v_max_f32_e32 v185, v176, v183
	v_min_f32_e32 v183, v176, v183
	v_max_f32_e32 v176, v184, v186
	v_min_f32_e32 v186, v184, v186
	v_max_f32_e32 v184, v176, v183
	v_min_f32_e32 v183, v176, v183
	v_max_f32_e32 v176, v181, v185
	v_min_f32_e32 v185, v181, v185
	v_max_f32_e32 v181, v179, v183
	v_min_f32_e32 v183, v179, v183
	v_max_f32_e32 v179, v181, v185
	v_min_f32_e32 v185, v181, v185
	v_max_f32_e32 v181, v180, v184
	v_min_f32_e32 v184, v180, v184
	v_max_f32_e32 v180, v182, v186
	v_min_f32_e32 v186, v182, v186
	v_max_f32_e32 v182, v180, v184
	v_min_f32_e32 v184, v180, v184
	v_max_f32_e32 v180, v181, v179
	v_min_f32_e32 v179, v181, v179
	v_max_f32_e32 v181, v182, v185
	v_min_f32_e32 v185, v182, v185
	v_max_f32_e32 v182, v184, v183
	v_min_f32_e32 v183, v184, v183
	v_max_f32_e32 v184, v187, v176
	v_min_f32_e32 v176, v187, v176
	v_max_f32_e32 v187, v177, v185
	v_min_f32_e32 v185, v177, v185
	v_max_f32_e32 v177, v187, v176
	v_min_f32_e32 v176, v187, v176
	v_max_f32_e32 v187, v149, v179
	v_min_f32_e32 v179, v149, v179
	v_max_f32_e32 v149, v175, v183
	v_min_f32_e32 v183, v175, v183
	v_max_f32_e32 v175, v149, v179
	v_min_f32_e32 v179, v149, v179
	v_max_f32_e32 v149, v187, v177
	v_min_f32_e32 v177, v187, v177
	v_max_f32_e32 v187, v175, v176
	v_min_f32_e32 v176, v175, v176
	v_max_f32_e32 v175, v179, v185
	v_min_f32_e32 v185, v179, v185
	v_max_f32_e32 v179, v172, v180
	v_min_f32_e32 v180, v172, v180
	v_max_f32_e32 v172, v174, v182
	v_min_f32_e32 v182, v174, v182
	v_max_f32_e32 v174, v172, v180
	v_min_f32_e32 v180, v172, v180
	v_max_f32_e32 v172, v173, v181
	v_min_f32_e32 v181, v173, v181
	v_max_f32_e32 v173, v178, v186
	v_min_f32_e32 v186, v178, v186
	v_max_f32_e32 v178, v173, v181
	v_min_f32_e32 v181, v173, v181
	v_max_f32_e32 v173, v172, v174
	v_min_f32_e32 v174, v172, v174
	v_max_f32_e32 v172, v178, v180
	v_min_f32_e32 v180, v178, v180
	v_max_f32_e32 v178, v181, v182
	v_min_f32_e32 v182, v181, v182
	v_max_f32_e32 v181, v179, v149
	v_min_f32_e32 v149, v179, v149
	v_max_f32_e32 v179, v173, v177
	v_min_f32_e32 v177, v173, v177
	v_max_f32_e32 v173, v174, v187
	v_min_f32_e32 v187, v174, v187
	v_max_f32_e32 v174, v172, v176
	v_min_f32_e32 v176, v172, v176
	v_max_f32_e32 v172, v180, v175
	v_min_f32_e32 v175, v180, v175
	v_max_f32_e32 v180, v178, v185
	v_min_f32_e32 v185, v178, v185
	v_max_f32_e32 v178, v182, v183
	v_min_f32_e32 v183, v182, v183
	v_max_f32_e32 v229, v229, v186
	v_max_f32_e32 v225, v225, v183
	v_max_f32_e32 v231, v231, v178
	v_max_f32_e32 v232, v232, v185
	v_max_f32_e32 v235, v235, v180
	v_max_f32_e32 v230, v230, v175
	v_max_f32_e32 v233, v233, v172
	v_max_f32_e32 v238, v238, v176
	v_max_f32_e32 v224, v224, v174
	v_max_f32_e32 v222, v222, v187
	v_max_f32_e32 v228, v228, v173
	v_max_f32_e32 v226, v226, v177
	v_max_f32_e32 v223, v223, v179
	v_max_f32_e32 v236, v236, v149
	v_max_f32_e32 v227, v227, v181
	v_max_f32_e32 v237, v237, v184
	v_max_f32_e32 v234, v229, v224
	v_min_f32_e32 v224, v229, v224
	v_max_f32_e32 v229, v225, v222
	v_min_f32_e32 v222, v225, v222
	v_max_f32_e32 v225, v231, v228
	v_min_f32_e32 v228, v231, v228
	v_max_f32_e32 v231, v232, v226
	v_min_f32_e32 v226, v232, v226
	v_max_f32_e32 v232, v235, v223
	v_min_f32_e32 v223, v235, v223
	v_max_f32_e32 v235, v230, v236
	v_min_f32_e32 v236, v230, v236
	v_max_f32_e32 v230, v233, v227
	v_min_f32_e32 v227, v233, v227
	v_max_f32_e32 v233, v238, v237
	v_min_f32_e32 v237, v238, v237
	v_max_f32_e32 v238, v234, v232
	v_min_f32_e32 v232, v234, v232
	v_max_f32_e32 v234, v229, v235
	v_min_f32_e32 v235, v229, v235
	v_max_f32_e32 v229, v225, v230
	v_min_f32_e32 v230, v225, v230
	v_max_f32_e32 v225, v231, v233
	v_min_f32_e32 v233, v231, v233
	v_max_f32_e32 v231, v224, v223
	v_min_f32_e32 v223, v224, v223
	v_max_f32_e32 v224, v222, v236
	v_min_f32_e32 v236, v222, v236
	v_max_f32_e32 v222, v228, v227
	v_min_f32_e32 v227, v228, v227
	v_max_f32_e32 v228, v226, v237
	v_min_f32_e32 v237, v226, v237
	v_max_f32_e32 v226, v238, v229
	v_min_f32_e32 v229, v238, v229
	v_max_f32_e32 v238, v234, v225
	v_min_f32_e32 v225, v234, v225
	v_max_f32_e32 v234, v232, v230
	v_min_f32_e32 v230, v232, v230
	v_max_f32_e32 v232, v235, v233
	v_min_f32_e32 v233, v235, v233
	v_max_f32_e32 v235, v231, v222
	v_min_f32_e32 v222, v231, v222
	v_max_f32_e32 v231, v224, v228
	v_min_f32_e32 v228, v224, v228
	v_max_f32_e32 v224, v223, v227
	v_min_f32_e32 v227, v223, v227
	v_max_f32_e32 v223, v236, v237
	v_min_f32_e32 v237, v236, v237
	v_max_f32_e32 v236, v226, v238
	v_min_f32_e32 v238, v226, v238
	v_max_f32_e32 v226, v229, v225
; __device__ __forceinline__ float uniq_key(float s, int n) { return __uint_as_float((__float_as_uint(s) & ~0xffu) | (unsigned)(255 - n)); }
; #define INS16(A_, X_) do { float x_ = (X_); _Pragma("unroll") for (int i_ = 0; i_ < 16; ++i_) { const float hi_ = fmaxf(A_[i_], x_); x_ = fminf(A_[i_], x_); A_[i_] = hi_; } } while (0)
; __device__ __forceinline__ void p11_route(Frame& F) {
;     ...
;             { int p = 0;
; #pragma unroll
;               for (int i = 0; i < 16; ++i)
; #pragma unroll
;                   for (int j = 0; j < 16; ++j) if ((i + 1) * (j + 1) <= 16) { INS16(b, uniq_key(v0[i] + v1[j], p)); ++p; } }
;             const int t = t0 + F.lane; float pv[16]; float den = 0.f; float mx = 0.f;
;             float rsn; { const f32x4* pp = (const f32x4*)((const float*)(F.ws + WS_PSQ) + (size_t)t * 64); float q = 0.f;
; #pragma unroll
;               for (int k = 0; k < 16; ++k) { const f32x4 a4 = pp[k]; q += (a4.x + a4.y) + (a4.z + a4.w); }
;               rsn = 1.0f / sqrtf(q * (1.f / D_) + 1e-6f); }
	v_min_f32_e32 v225, v229, v225
	v_max_f32_e32 v229, v234, v232
	v_min_f32_e32 v232, v234, v232
	v_max_f32_e32 v234, v230, v233
	v_min_f32_e32 v233, v230, v233
	v_max_f32_e32 v230, v235, v231
	v_min_f32_e32 v231, v235, v231
	v_max_f32_e32 v235, v222, v228
	v_min_f32_e32 v228, v222, v228
	v_max_f32_e32 v222, v224, v223
	v_min_f32_e32 v223, v224, v223
	v_max_f32_e32 v224, v227, v237
	v_min_f32_e32 v237, v227, v237
	v_add_f32_e32 v149, v140, v142
	v_and_b32_e32 v149, 0xffffff00, v149
	v_or_b32_e32 v149, 0xcf, v149
	v_max_f32_e32 v227, v236, v149
	v_min_f32_e32 v236, v236, v149
	v_max_f32_e32 v149, v238, v236
	v_min_f32_e32 v238, v238, v236
	v_max_f32_e32 v236, v226, v238
	v_min_f32_e32 v226, v226, v238
	v_max_f32_e32 v238, v225, v226
	v_min_f32_e32 v225, v225, v226
	v_max_f32_e32 v226, v229, v225
	v_min_f32_e32 v229, v229, v225
	v_max_f32_e32 v225, v232, v229
	v_min_f32_e32 v232, v232, v229
	v_max_f32_e32 v229, v234, v232
	v_min_f32_e32 v234, v234, v232
	v_max_f32_e32 v232, v233, v234
	v_min_f32_e32 v233, v233, v234
	v_max_f32_e32 v234, v230, v233
	v_min_f32_e32 v230, v230, v233
	v_max_f32_e32 v233, v231, v230
	v_min_f32_e32 v231, v231, v230
	v_max_f32_e32 v230, v235, v231
	v_min_f32_e32 v235, v235, v231
	v_max_f32_e32 v231, v228, v235
	v_min_f32_e32 v228, v228, v235
	v_max_f32_e32 v235, v222, v228
	v_min_f32_e32 v222, v222, v228
	v_max_f32_e32 v228, v223, v222
	v_min_f32_e32 v223, v223, v222
	v_max_f32_e32 v222, v224, v223
	v_min_f32_e32 v224, v224, v223
	v_max_f32_e32 v237, v237, v224
	v_add_f32_e32 v172, v141, v142
	v_and_b32_e32 v172, 0xffffff00, v172
	v_or_b32_e32 v172, 0xce, v172
	v_max_f32_e32 v223, v227, v172
	v_min_f32_e32 v227, v227, v172
	v_max_f32_e32 v172, v149, v227
	v_min_f32_e32 v149, v149, v227
	v_max_f32_e32 v227, v236, v149
	v_min_f32_e32 v236, v236, v149
	v_max_f32_e32 v149, v238, v236
	v_min_f32_e32 v238, v238, v236
	v_max_f32_e32 v236, v226, v238
	v_min_f32_e32 v226, v226, v238
	v_max_f32_e32 v238, v225, v226
	v_min_f32_e32 v225, v225, v226
	v_max_f32_e32 v226, v229, v225
	v_min_f32_e32 v229, v229, v225
	v_max_f32_e32 v225, v232, v229
	v_min_f32_e32 v232, v232, v229
	v_max_f32_e32 v229, v234, v232
	v_min_f32_e32 v234, v234, v232
	v_max_f32_e32 v232, v233, v234
	v_min_f32_e32 v233, v233, v234
	v_max_f32_e32 v234, v230, v233
	v_min_f32_e32 v230, v230, v233
	v_max_f32_e32 v233, v231, v230
	v_min_f32_e32 v231, v231, v230
	v_max_f32_e32 v230, v235, v231
	v_min_f32_e32 v235, v235, v231
	v_max_f32_e32 v231, v228, v235
	v_min_f32_e32 v228, v228, v235
	v_max_f32_e32 v235, v222, v228
	v_min_f32_e32 v222, v222, v228
	v_max_f32_e32 v237, v237, v222
	v_mov_b32_e32 v212, v223
	v_mov_b32_e32 v213, v172
	v_mov_b32_e32 v214, v227
	v_mov_b32_e32 v215, v149
	v_mov_b32_e32 v216, v236
	v_mov_b32_e32 v217, v238
	v_mov_b32_e32 v218, v226
	v_mov_b32_e32 v219, v225
	v_mov_b32_e32 v221, v229
	v_mov_b32_e32 v211, v232
	v_mov_b32_e32 v210, v234
	v_mov_b32_e32 v159, v233
	v_mov_b32_e32 v220, v230
	v_add_u32_e32 v130, s18, v1
	v_ashrrev_i32_e32 v131, 31, v130
	v_lshlrev_b64 v[132:133], 8, v[130:131]
	v_lshl_add_u64 v[148:149], s[6:7], 0, v[132:133]
	global_load_dwordx4 v[132:135], v[148:149], off offset:16
	global_load_dwordx4 v[136:139], v[148:149], off
	global_load_dwordx4 v[140:143], v[148:149], off offset:48
	global_load_dwordx4 v[144:147], v[148:149], off offset:32
	global_load_dwordx4 v[160:163], v[148:149], off offset:80
	global_load_dwordx4 v[164:167], v[148:149], off offset:64
	global_load_dwordx4 v[168:171], v[148:149], off offset:112
	global_load_dwordx4 v[172:175], v[148:149], off offset:96
	global_load_dwordx4 v[176:179], v[148:149], off offset:144
	global_load_dwordx4 v[180:183], v[148:149], off offset:128
	global_load_dwordx4 v[126:129], v[148:149], off offset:176
	global_load_dwordx4 v[184:187], v[148:149], off offset:160
	global_load_dwordx4 v[188:191], v[148:149], off offset:208
	global_load_dwordx4 v[192:195], v[148:149], off offset:192
	global_load_dwordx4 v[196:199], v[148:149], off offset:240
	global_load_dwordx4 v[200:203], v[148:149], off offset:224
	s_waitcnt vmcnt(14)
	v_mov_b32_e32 v148, v137
	v_mov_b32_e32 v149, v138
	v_mov_b32_e32 v137, v139
	v_mov_b32_e32 v138, v133
	v_mov_b32_e32 v139, v134
	v_mov_b32_e32 v133, v135
	v_pk_add_f32 v[136:137], v[148:149], v[136:137]
	v_pk_add_f32 v[132:133], v[138:139], v[132:133]
	v_add_f32_e32 v136, v136, v137
	v_pk_add_f32 v[132:133], v[132:133], v[132:133] op_sel:[0,1] op_sel_hi:[1,0]
	v_add_f32_e32 v136, 0, v136
	s_waitcnt vmcnt(13)
	v_mov_b32_e32 v137, v140
	s_waitcnt vmcnt(12)
	v_add_f32_e32 v134, v144, v145
	v_add_f32_e32 v138, v146, v147
	v_mov_b32_e32 v133, v141
	v_mov_b32_e32 v135, v142
	v_mov_b32_e32 v139, v143
	v_pk_add_f32 v[132:133], v[136:137], v[132:133]
	v_pk_add_f32 v[134:135], v[134:135], v[138:139]
	s_waitcnt vmcnt(11)
	v_add_f32_e32 v136, v160, v161
	v_pk_add_f32 v[132:133], v[132:133], v[134:135]
	s_waitcnt vmcnt(10)
	v_mov_b32_e32 v134, v165
	v_mov_b32_e32 v135, v166
	v_mov_b32_e32 v165, v167
	v_pk_add_f32 v[134:135], v[134:135], v[164:165]
	v_pk_add_f32 v[132:133], v[132:133], v[132:133] op_sel:[0,1] op_sel_hi:[1,0]
	v_pk_add_f32 v[134:135], v[134:135], v[134:135] op_sel:[0,1] op_sel_hi:[1,0]
	v_add_f32_e32 v138, v162, v163
	s_waitcnt vmcnt(8)
	v_mov_b32_e32 v133, v172
	v_mov_b32_e32 v135, v173
	v_mov_b32_e32 v137, v174
	v_mov_b32_e32 v139, v175
	v_pk_add_f32 v[132:133], v[132:133], v[134:135]
	v_pk_add_f32 v[134:135], v[136:137], v[138:139]
	s_waitcnt vmcnt(7)
	v_mov_b32_e32 v137, v178
	v_pk_add_f32 v[132:133], v[132:133], v[134:135]
	v_mov_b32_e32 v134, v169
	v_mov_b32_e32 v135, v170
	v_mov_b32_e32 v169, v171
	v_pk_add_f32 v[134:135], v[134:135], v[168:169]
	v_pk_add_f32 v[132:133], v[132:133], v[132:133] op_sel:[0,1] op_sel_hi:[1,0]
	v_pk_add_f32 v[134:135], v[134:135], v[134:135] op_sel:[0,1] op_sel_hi:[1,0]
	s_waitcnt vmcnt(6)
; __device__ __forceinline__ void p11_route(Frame& F) {
;     ...
;             float rsn; { const f32x4* pp = (const f32x4*)((const float*)(F.ws + WS_PSQ) + (size_t)t * 64); float q = 0.f;
; #pragma unroll
;               for (int k = 0; k < 16; ++k) { const f32x4 a4 = pp[k]; q += (a4.x + a4.y) + (a4.z + a4.w); }
;               rsn = 1.0f / sqrtf(q * (1.f / D_) + 1e-6f); }
; #pragma unroll
;             for (int r = 0; r < 16; ++r) { const int p = 255 - (int)(__float_as_uint(b[r]) & 255u); const int ij = ptab[p]; const int ii = ij >> 4, jj = ij & 15;
;                 const float val = r0[ii] + r1[jj]; if (r == 0) mx = val; pv[r] = __expf((val - mx) * rsn); den += pv[r];
;                 PIDX[(size_t)t * 128 + h * PT + r] = __float_as_int(r0[16 + ii]) * PNK + __float_as_int(r1[16 + jj]); }
	v_add_f32_e32 v136, v180, v181
	v_add_f32_e32 v138, v182, v183
	v_mov_b32_e32 v133, v176
	v_mov_b32_e32 v135, v177
	v_mov_b32_e32 v139, v179
	v_pk_add_f32 v[132:133], v[132:133], v[134:135]
	v_pk_add_f32 v[134:135], v[136:137], v[138:139]
	s_waitcnt vmcnt(5)
	v_add_f32_e32 v126, v126, v127
	v_pk_add_f32 v[132:133], v[132:133], v[134:135]
	s_waitcnt vmcnt(4)
	v_mov_b32_e32 v134, v185
	v_mov_b32_e32 v135, v186
	v_mov_b32_e32 v185, v187
	v_pk_add_f32 v[134:135], v[134:135], v[184:185]
	v_pk_add_f32 v[132:133], v[132:133], v[132:133] op_sel:[0,1] op_sel_hi:[1,0]
	v_pk_add_f32 v[134:135], v[134:135], v[134:135] op_sel:[0,1] op_sel_hi:[1,0]
	v_add_f32_e32 v128, v128, v129
	s_waitcnt vmcnt(2)
	v_mov_b32_e32 v133, v192
	v_mov_b32_e32 v135, v193
	v_mov_b32_e32 v127, v194
	v_mov_b32_e32 v129, v195
	v_pk_add_f32 v[132:133], v[132:133], v[134:135]
	v_pk_add_f32 v[126:127], v[126:127], v[128:129]
	v_mov_b32_e32 v128, v189
	v_mov_b32_e32 v129, v190
	v_mov_b32_e32 v189, v191
	v_pk_add_f32 v[126:127], v[132:133], v[126:127]
	v_pk_add_f32 v[128:129], v[128:129], v[188:189]
	v_pk_add_f32 v[126:127], v[126:127], v[126:127] op_sel:[0,1] op_sel_hi:[1,0]
	v_pk_add_f32 v[128:129], v[128:129], v[128:129] op_sel:[0,1] op_sel_hi:[1,0]
	s_waitcnt vmcnt(0)
	v_add_f32_e32 v132, v200, v201
	v_add_f32_e32 v134, v202, v203
	v_mov_b32_e32 v127, v196
	v_mov_b32_e32 v129, v197
	v_mov_b32_e32 v133, v198
	v_mov_b32_e32 v135, v199
	v_pk_add_f32 v[126:127], v[126:127], v[128:129]
	v_pk_add_f32 v[128:129], v[132:133], v[134:135]
	v_xor_b32_e32 v136, -1, v219
	v_pk_add_f32 v[126:127], v[126:127], v[128:129]
	v_add_f32_e32 v126, v126, v127
	v_fmamk_f32 v126, v126, 0x39800000, v157
	v_mul_f32_e32 v127, 0x4f800000, v126
	v_cmp_gt_f32_e32 vcc, s15, v126
	v_cndmask_b32_e32 v126, v126, v127, vcc
	v_sqrt_f32_e32 v127, v126
	v_mov_b32_e32 v146, v231
	v_mov_b32_e32 v147, v235
	v_mov_b32_e32 v148, v237
	v_add_u32_e32 v129, -1, v127
	v_fma_f32 v132, -v129, v127, v126
	v_cmp_ge_f32_e64 s[4:5], 0, v132
	v_add_u32_e32 v132, 1, v127
	v_xor_b32_e32 v134, -1, v217
	v_cndmask_b32_e64 v129, v127, v129, s[4:5]
	v_fma_f32 v127, -v132, v127, v126
	v_cmp_lt_f32_e64 s[4:5], 0, v127
	v_xor_b32_e32 v135, -1, v216
	v_xor_b32_e32 v137, -1, v218
	v_cndmask_b32_e64 v127, v129, v132, s[4:5]
	v_mul_f32_e32 v129, 0x37800000, v127
	v_cndmask_b32_e32 v127, v127, v129, vcc
	v_cmp_class_f32_e32 vcc, v126, v158
	v_and_b32_e32 v136, 0xff, v136
	v_and_b32_e32 v134, 0xff, v134
	v_cndmask_b32_e32 v126, v127, v126, vcc
	v_div_scale_f32 v127, s[4:5], v126, v126, 1.0
	v_rcp_f32_e32 v129, v127
	v_and_b32_e32 v135, 0xff, v135
	v_and_b32_e32 v137, 0xff, v137
	v_lshl_add_u32 v136, v136, 2, s16
	v_fma_f32 v128, -v127, v129, 1.0
	v_fmac_f32_e32 v129, v128, v129
	v_div_scale_f32 v128, vcc, 1.0, v126, 1.0
	v_mul_f32_e32 v132, v128, v129
	v_fma_f32 v133, -v127, v132, v128
	v_fmac_f32_e32 v132, v133, v129
	v_fma_f32 v127, -v127, v132, v128
	v_div_fmas_f32 v127, v127, v129, v132
	v_div_fixup_f32 v167, v127, v126, 1.0
	v_lshlrev_b64 v[126:127], 9, v[130:131]
	v_xor_b32_e32 v131, -1, v212
	v_xor_b32_e32 v132, -1, v215
	v_xor_b32_e32 v130, -1, v213
	v_and_b32_e32 v131, 0xff, v131
	v_xor_b32_e32 v133, -1, v214
	v_and_b32_e32 v132, 0xff, v132
	v_and_b32_e32 v130, 0xff, v130
	v_lshl_add_u32 v131, v131, 2, s16
	v_and_b32_e32 v133, 0xff, v133
	v_lshl_add_u32 v132, v132, 2, s16
	v_lshl_add_u32 v130, v130, 2, s16
	v_lshl_add_u32 v133, v133, 2, s16
	v_lshl_add_u32 v135, v135, 2, s16
	v_lshl_add_u32 v134, v134, 2, s16
	v_lshl_add_u32 v137, v137, 2, s16
	ds_read_b32 v131, v131
	ds_read_b32 v138, v130
	ds_read_b32 v139, v133
	ds_read_b32 v142, v132
	ds_read_b32 v149, v135
	ds_read_b32 v160, v134
	ds_read_b32 v161, v137
	ds_read_b32 v162, v136
	s_waitcnt lgkmcnt(7)
	v_and_b32_e32 v132, 15, v131
	s_waitcnt lgkmcnt(6)
	v_and_b32_e32 v136, 15, v138
	v_ashrrev_i32_e32 v130, 4, v131
	v_lshl_add_u32 v132, v132, 2, v154
	v_ashrrev_i32_e32 v134, 4, v138
	v_lshl_add_u32 v136, v136, 2, v154
	s_waitcnt lgkmcnt(5)
	v_and_b32_e32 v140, 15, v139
	s_waitcnt lgkmcnt(4)
	v_and_b32_e32 v144, 15, v142
	v_lshl_add_u32 v130, v130, 2, v154
	v_add_u32_e32 v132, 0x2000, v132
	v_lshl_add_u32 v134, v134, 2, v154
	v_add_u32_e32 v136, 0x2000, v136
	v_ashrrev_i32_e32 v138, 4, v139
	v_lshl_add_u32 v140, v140, 2, v154
	v_ashrrev_i32_e32 v143, 4, v142
	v_lshl_add_u32 v144, v144, 2, v154
	ds_read2_b32 v[130:131], v130 offset1:16
	ds_read2_b32 v[132:133], v132 offset0:16 offset1:32
	ds_read2_b32 v[134:135], v134 offset1:16
	ds_read2_b32 v[136:137], v136 offset0:16 offset1:32
	v_lshl_add_u32 v138, v138, 2, v154
	v_add_u32_e32 v140, 0x2000, v140
	v_lshl_add_u32 v142, v143, 2, v154
	v_add_u32_e32 v144, 0x2000, v144
	ds_read2_b32 v[138:139], v138 offset1:16
	ds_read2_b32 v[140:141], v140 offset0:16 offset1:32
	ds_read2_b32 v[142:143], v142 offset1:16
	ds_read2_b32 v[144:145], v144 offset0:16 offset1:32
	s_waitcnt lgkmcnt(4)
	v_add_f32_e32 v164, v134, v136
	v_lshl_add_u32 v134, v131, 7, v133
	v_ashrrev_i32_e32 v131, 4, v149
	v_lshl_add_u64 v[128:129], s[8:9], 0, v[126:127]
	v_lshl_add_u32 v135, v135, 7, v137
	s_waitcnt lgkmcnt(0)
	v_lshl_add_u32 v137, v143, 7, v145
	v_lshl_add_u32 v136, v139, 7, v141
	v_and_b32_e32 v133, 15, v149
	v_lshl_add_u32 v131, v131, 2, v154
	global_store_dwordx4 v[128:129], v[134:137], off
	ds_read2_b32 v[136:137], v131 offset1:16
	v_lshl_add_u32 v131, v133, 2, v154
	v_add_u32_e32 v131, 0x2000, v131
	v_add_f32_e32 v165, v138, v140
	ds_read2_b32 v[138:139], v131 offset0:16 offset1:32
	v_ashrrev_i32_e32 v131, 4, v160
	v_and_b32_e32 v133, 15, v160
	v_lshl_add_u32 v131, v131, 2, v154
	ds_read2_b32 v[134:135], v131 offset1:16
	v_lshl_add_u32 v131, v133, 2, v154
	v_add_u32_e32 v131, 0x2000, v131
	ds_read2_b32 v[140:141], v131 offset0:16 offset1:32
	v_ashrrev_i32_e32 v131, 4, v161
	v_and_b32_e32 v133, 15, v161
	v_lshl_add_u32 v131, v131, 2, v154
	v_add_f32_e32 v166, v142, v144
	ds_read2_b32 v[142:143], v131 offset1:16
	v_lshl_add_u32 v131, v133, 2, v154
	v_add_u32_e32 v131, 0x2000, v131
	ds_read2_b32 v[144:145], v131 offset0:16 offset1:32
	v_ashrrev_i32_e32 v131, 4, v162
	v_and_b32_e32 v133, 15, v162
	v_lshl_add_u32 v131, v131, 2, v154
	s_waitcnt lgkmcnt(4)
; __device__ __forceinline__ void p11_route(Frame& F) {
;     ...
;             for (int r = 0; r < 16; ++r) { const int p = 255 - (int)(__float_as_uint(b[r]) & 255u); const int ij = ptab[p]; const int ii = ij >> 4, jj = ij & 15;
;                 const float val = r0[ii] + r1[jj]; if (r == 0) mx = val; pv[r] = __expf((val - mx) * rsn); den += pv[r];
;                 PIDX[(size_t)t * 128 + h * PT + r] = __float_as_int(r0[16 + ii]) * PNK + __float_as_int(r1[16 + jj]); }
	v_add_f32_e32 v168, v136, v138
	s_waitcnt lgkmcnt(2)
	v_add_f32_e32 v169, v134, v140
	v_lshl_add_u32 v134, v137, 7, v139
	ds_read2_b32 v[136:137], v131 offset1:16
	v_lshl_add_u32 v131, v133, 2, v154
	v_add_u32_e32 v131, 0x2000, v131
	ds_read2_b32 v[138:139], v131 offset0:16 offset1:32
	v_xor_b32_e32 v131, -1, v211
	v_xor_b32_e32 v133, -1, v221
	v_lshl_add_u32 v135, v135, 7, v141
	s_waitcnt lgkmcnt(2)
	v_add_f32_e32 v170, v142, v144
	v_and_b32_e32 v131, 0xff, v131
	v_and_b32_e32 v133, 0xff, v133
	v_xor_b32_e32 v140, -1, v159
	v_xor_b32_e32 v141, -1, v210
	v_xor_b32_e32 v142, -1, v146
	v_xor_b32_e32 v144, -1, v220
	v_xor_b32_e32 v146, -1, v148
	v_xor_b32_e32 v147, -1, v147
	v_lshl_add_u32 v133, v133, 2, s16
	v_lshl_add_u32 v131, v131, 2, s16
	v_and_b32_e32 v140, 0xff, v140
	v_and_b32_e32 v141, 0xff, v141
	v_and_b32_e32 v142, 0xff, v142
	v_and_b32_e32 v144, 0xff, v144
	v_and_b32_e32 v146, 0xff, v146
	v_and_b32_e32 v147, 0xff, v147
	v_lshl_add_u32 v141, v141, 2, s16
	v_lshl_add_u32 v140, v140, 2, s16
	v_lshl_add_u32 v144, v144, 2, s16
	v_lshl_add_u32 v142, v142, 2, s16
	v_lshl_add_u32 v147, v147, 2, s16
	v_lshl_add_u32 v146, v146, 2, s16
	ds_read_b32 v133, v133
	ds_read_b32 v131, v131
	ds_read_b32 v148, v141
	ds_read_b32 v149, v140
	ds_read_b32 v159, v144
	ds_read_b32 v160, v142
	ds_read_b32 v171, v147
	ds_read_b32 v172, v146
	s_waitcnt lgkmcnt(7)
	v_ashrrev_i32_e32 v140, 4, v133
	v_and_b32_e32 v133, 15, v133
	v_lshl_add_u32 v133, v133, 2, v154
	v_add_u32_e32 v133, 0x2000, v133
	ds_read2_b32 v[146:147], v133 offset0:16 offset1:32
	s_waitcnt lgkmcnt(7)
	v_ashrrev_i32_e32 v133, 4, v131
	v_and_b32_e32 v131, 15, v131
	v_lshl_add_u32 v131, v131, 2, v154
	v_add_f32_e32 v173, v136, v138
	v_lshl_add_u32 v137, v137, 7, v139
	v_lshl_add_u32 v136, v143, 7, v145
	v_add_u32_e32 v131, 0x2000, v131
	global_store_dwordx4 v[128:129], v[134:137], off offset:16
	v_lshl_add_u32 v133, v133, 2, v154
	ds_read2_b32 v[136:137], v131 offset0:16 offset1:32
	s_waitcnt lgkmcnt(7)
	v_ashrrev_i32_e32 v131, 4, v148
	ds_read2_b32 v[134:135], v133 offset1:16
	v_and_b32_e32 v133, 15, v148
	v_lshl_add_u32 v131, v131, 2, v154
	ds_read2_b32 v[138:139], v131 offset1:16
	v_lshl_add_u32 v131, v133, 2, v154
	v_add_u32_e32 v131, 0x2000, v131
	v_lshl_add_u32 v140, v140, 2, v154
	ds_read2_b32 v[142:143], v131 offset0:16 offset1:32
	s_waitcnt lgkmcnt(9)
	v_ashrrev_i32_e32 v131, 4, v149
	ds_read2_b32 v[140:141], v140 offset1:16
	v_and_b32_e32 v133, 15, v149
	v_lshl_add_u32 v131, v131, 2, v154
	ds_read2_b32 v[144:145], v131 offset1:16
	v_lshl_add_u32 v131, v133, 2, v154
	v_add_u32_e32 v131, 0x2000, v131
	ds_read2_b32 v[148:149], v131 offset0:16 offset1:32
	s_waitcnt lgkmcnt(11)
	v_ashrrev_i32_e32 v131, 4, v159
	v_and_b32_e32 v133, 15, v159
	v_lshl_add_u32 v131, v131, 2, v154
	s_waitcnt lgkmcnt(2)
	v_add_f32_e32 v174, v140, v146
	v_add_f32_e32 v175, v134, v136
	v_lshl_add_u32 v134, v141, 7, v147
	ds_read2_b32 v[140:141], v131 offset1:16
	v_lshl_add_u32 v131, v133, 2, v154
	v_add_u32_e32 v131, 0x2000, v131
	ds_read2_b32 v[146:147], v131 offset0:16 offset1:32
	v_ashrrev_i32_e32 v131, 4, v160
	v_and_b32_e32 v133, 15, v160
	v_lshl_add_u32 v131, v131, 2, v154
	ds_read2_b32 v[160:161], v131 offset1:16
	v_lshl_add_u32 v131, v133, 2, v154
	v_add_u32_e32 v131, 0x2000, v131
	ds_read2_b32 v[162:163], v131 offset0:16 offset1:32
	v_ashrrev_i32_e32 v131, 4, v171
	v_and_b32_e32 v133, 15, v171
	v_lshl_add_u32 v131, v131, 2, v154
	v_add_f32_e32 v176, v138, v142
	v_lshl_add_u32 v136, v139, 7, v143
	ds_read2_b32 v[138:139], v131 offset1:16
	v_lshl_add_u32 v131, v133, 2, v154
	v_add_u32_e32 v131, 0x2000, v131
	ds_read2_b32 v[142:143], v131 offset0:16 offset1:32
	v_ashrrev_i32_e32 v131, 4, v172
	v_lshl_add_u32 v135, v135, 7, v137
	s_waitcnt lgkmcnt(6)
	v_lshl_add_u32 v137, v145, 7, v149
	v_and_b32_e32 v133, 15, v172
	v_lshl_add_u32 v131, v131, 2, v154
	global_store_dwordx4 v[128:129], v[134:137], off offset:32
	ds_read2_b32 v[136:137], v131 offset1:16
	v_lshl_add_u32 v131, v133, 2, v154
	v_add_u32_e32 v131, 0x2000, v131
	v_add_f32_e32 v177, v144, v148
	ds_read2_b32 v[144:145], v131 offset0:16 offset1:32
	s_waitcnt lgkmcnt(6)
	v_add_f32_e32 v159, v140, v146
	v_lshl_add_u32 v134, v141, 7, v147
	s_waitcnt lgkmcnt(1)
; __device__ __forceinline__ void p11_route(Frame& F) {
;     ...
;             for (int r = 0; r < 16; ++r) { const int p = 255 - (int)(__float_as_uint(b[r]) & 255u); const int ij = ptab[p]; const int ii = ij >> 4, jj = ij & 15;
;                 const float val = r0[ii] + r1[jj]; if (r == 0) mx = val; pv[r] = __expf((val - mx) * rsn); den += pv[r];
;                 PIDX[(size_t)t * 128 + h * PT + r] = __float_as_int(r0[16 + ii]) * PNK + __float_as_int(r1[16 + jj]); }
;             const float inv = 1.0f / den;
; #pragma unroll
;             for (int r = 0; r < 16; ++r) PGT[(size_t)t * 128 + h * PT + r] = pv[r] * inv;
	v_mov_b32_e32 v140, v136
	v_mov_b32_e32 v141, v130
	s_waitcnt lgkmcnt(0)
	v_mov_b32_e32 v130, v144
	v_mov_b32_e32 v131, v132
	v_pk_add_f32 v[130:131], v[140:141], v[130:131]
	v_add_f32_e32 v138, v138, v142
	v_sub_f32_e32 v142, v168, v131
	v_mul_f32_e32 v142, v167, v142
	v_mul_f32_e32 v142, 0x3fb8aa3b, v142
	v_exp_f32_e32 v146, v142
	v_sub_f32_e32 v142, v169, v131
	v_mul_f32_e32 v142, v167, v142
	v_mul_f32_e32 v142, 0x3fb8aa3b, v142
	v_exp_f32_e32 v147, v142
	v_sub_f32_e32 v142, v170, v131
	v_mul_f32_e32 v142, v167, v142
	v_mul_f32_e32 v142, 0x3fb8aa3b, v142
	v_exp_f32_e32 v148, v142
	v_sub_f32_e32 v142, v173, v131
	v_mul_f32_e32 v142, v167, v142
	v_mul_f32_e32 v142, 0x3fb8aa3b, v142
	v_exp_f32_e32 v149, v142
	v_sub_f32_e32 v142, v174, v131
	v_mul_f32_e32 v142, v167, v142
	v_sub_f32_e32 v132, v131, v131
	v_sub_f32_e32 v136, v165, v131
	v_mul_f32_e32 v142, 0x3fb8aa3b, v142
	v_add_f32_e32 v178, v160, v162
	v_mul_f32_e32 v132, v132, v167
	v_sub_f32_e32 v133, v164, v131
	v_mul_f32_e32 v136, v167, v136
	v_exp_f32_e32 v160, v142
	v_sub_f32_e32 v142, v175, v131
	v_mul_f32_e32 v132, 0x3fb8aa3b, v132
	v_mul_f32_e32 v133, v167, v133
	v_mul_f32_e32 v136, 0x3fb8aa3b, v136
	v_mul_f32_e32 v142, v167, v142
	v_exp_f32_e32 v132, v132
	v_mul_f32_e32 v133, 0x3fb8aa3b, v133
	v_exp_f32_e32 v140, v136
	v_sub_f32_e32 v136, v166, v131
	v_mul_f32_e32 v142, 0x3fb8aa3b, v142
	v_lshl_add_u32 v135, v161, 7, v163
	v_exp_f32_e32 v133, v133
	v_mul_f32_e32 v136, v167, v136
	v_exp_f32_e32 v161, v142
	v_sub_f32_e32 v142, v176, v131
	v_mul_f32_e32 v136, 0x3fb8aa3b, v136
	v_mul_f32_e32 v142, v167, v142
	v_exp_f32_e32 v141, v136
	v_mul_f32_e32 v142, 0x3fb8aa3b, v142
	v_add_f32_e32 v136, 0, v132
	v_exp_f32_e32 v162, v142
	v_sub_f32_e32 v142, v177, v131
	v_add_f32_e32 v136, v136, v133
	v_mul_f32_e32 v142, v167, v142
	v_add_f32_e32 v136, v136, v140
	v_mul_f32_e32 v142, 0x3fb8aa3b, v142
	v_add_f32_e32 v136, v136, v141
	v_exp_f32_e32 v163, v142
	v_sub_f32_e32 v142, v159, v131
	v_add_f32_e32 v136, v136, v146
	v_mul_f32_e32 v142, v167, v142
	v_add_f32_e32 v136, v136, v147
	v_mul_f32_e32 v142, 0x3fb8aa3b, v142
	v_add_f32_e32 v136, v136, v148
	v_exp_f32_e32 v164, v142
	v_sub_f32_e32 v142, v178, v131
	v_add_f32_e32 v136, v136, v149
	v_mul_f32_e32 v142, v167, v142
	v_sub_f32_e32 v138, v138, v131
	v_add_f32_e32 v136, v136, v160
	v_mul_f32_e32 v142, 0x3fb8aa3b, v142
	v_mul_f32_e32 v138, v167, v138
	v_sub_f32_e32 v130, v130, v131
	v_add_f32_e32 v136, v136, v161
	v_exp_f32_e32 v165, v142
	v_mul_f32_e32 v138, 0x3fb8aa3b, v138
	v_mul_f32_e32 v130, v167, v130
	v_add_f32_e32 v136, v136, v162
	v_exp_f32_e32 v166, v138
	v_mul_f32_e32 v130, 0x3fb8aa3b, v130
	v_add_f32_e32 v136, v136, v163
	v_exp_f32_e32 v167, v130
	v_add_f32_e32 v130, v136, v164
	v_add_f32_e32 v130, v130, v165
	v_add_f32_e32 v130, v130, v166
	v_add_f32_e32 v130, v130, v167
	v_div_scale_f32 v131, s[4:5], v130, v130, 1.0
	v_rcp_f32_e32 v138, v131
	v_lshl_add_u32 v137, v137, 7, v145
	v_lshl_add_u32 v136, v139, 7, v143
	global_store_dwordx4 v[128:129], v[134:137], off offset:48
	v_fma_f32 v128, -v131, v138, 1.0
	v_fmac_f32_e32 v138, v128, v138
	v_div_scale_f32 v128, vcc, 1.0, v130, 1.0
	v_mul_f32_e32 v129, v128, v138
	v_fma_f32 v134, -v131, v129, v128
	v_fmac_f32_e32 v129, v134, v138
	v_fma_f32 v128, -v131, v129, v128
	v_div_fmas_f32 v128, v128, v138, v129
	v_div_fixup_f32 v130, v128, v130, 1.0
	v_lshl_add_u64 v[134:135], s[10:11], 0, v[126:127]
	v_pk_mul_f32 v[126:127], v[132:133], v[130:131] op_sel_hi:[1,0]
	v_pk_mul_f32 v[128:129], v[140:141], v[130:131] op_sel_hi:[1,0]
	global_store_dwordx4 v[134:135], v[126:129], off
	s_nop 1
	v_pk_mul_f32 v[126:127], v[146:147], v[130:131] op_sel_hi:[1,0]
	v_pk_mul_f32 v[128:129], v[148:149], v[130:131] op_sel_hi:[1,0]
	global_store_dwordx4 v[134:135], v[126:129], off offset:16
	s_nop 1
	v_pk_mul_f32 v[126:127], v[160:161], v[130:131] op_sel_hi:[1,0]
	v_pk_mul_f32 v[128:129], v[162:163], v[130:131] op_sel_hi:[1,0]
	global_store_dwordx4 v[134:135], v[126:129], off offset:32
	s_nop 1
	v_pk_mul_f32 v[126:127], v[164:165], v[130:131] op_sel_hi:[1,0]
	v_pk_mul_f32 v[128:129], v[166:167], v[130:131] op_sel_hi:[1,0]
	global_store_dwordx4 v[134:135], v[126:129], off offset:48
	s_branch .LBB0_3213
